# baseline (speedup 1.0000x reference)
.LBB1_7:
	s_or_b64 exec, exec, s[2:3]
	v_mov_b32_e32 v10, v167
	s_waitcnt lgkmcnt(0)
	s_barrier
	s_waitcnt vmcnt(18)
	s_ashr_i32 s2, s4, 6
	s_lshl_b32 s3, s2, 3
	s_and_b32 s5, s3, 8
	s_bfe_u32 s26, s2, 0x10001
	s_or_b32 s5, s26, s5
	s_lshl_b32 s26, s2, 9
	s_and_b32 s26, s26, 0x400
	s_lshl_b32 s5, s5, 4
	s_or_b32 s28, s5, s26
	v_lshrrev_b32_e32 v182, 5, v167
	v_bfe_u32 v2, v156, 4, 1
	v_bitop3_b32 v3, v182, v156, 1 bitop3:0x78
	v_lshlrev_b32_e32 v154, 2, v182
	v_xor_b32_e32 v3, v3, v2
	v_bitop3_b32 v4, v154, v156, 4 bitop3:0x78
	v_and_b32_e32 v5, 10, v156
	v_or3_b32 v3, v5, v4, v3
	s_lshl_b32 s5, s2, 4
	v_lshlrev_b32_e32 v3, 4, v3
	s_lshl_b32 s3, s2, 13
	s_and_b32 s29, s5, 16
	v_lshlrev_b32_e32 v170, 8, v182
	v_lshl_or_b32 v171, v2, 10, v3
	s_or_b32 s26, s29, s3
	v_bitop3_b32 v179, v171, s26, v170 bitop3:0x36
	s_or_b32 s5, s26, 0x280
	v_bitop3_b32 v178, v171, s5, v170 bitop3:0x36
	s_or_b32 s30, s3, 0x800
	s_or_b32 s33, s3, 0x1000
	s_or_b32 s29, s29, 64
	s_or_b32 s34, s29, s33
	v_bitop3_b32 v180, v171, s34, v170 bitop3:0x36
	s_or_b32 s29, s3, s29
	s_or_b32 s29, s29, 0x1280
	s_and_b32 s5, s2, 1
	s_lshl_b32 s31, s5, 4
	s_or_b32 s2, s31, s3
	v_bitop3_b32 v173, v171, s2, v170 bitop3:0x36
	v_bitop3_b32 v34, v156, 31, v156 bitop3:0xc
	v_lshrrev_b32_e32 v35, 4, v34
	v_bitop3_b32 v36, v34, v182, 1 bitop3:0x6c
	v_xor_b32_e32 v36, v36, v35
	v_bitop3_b32 v34, v34, v154, 4 bitop3:0x6c
	v_bitop3_b32 v37, v156, 10, 31 bitop3:8
	v_or3_b32 v34, v37, v34, v36
	v_lshlrev_b32_e32 v35, 10, v35
	v_lshlrev_b32_e32 v34, 4, v34
	v_or3_b32 v154, v35, v34, v170
	v_bitop3_b32 v172, s2, v154, v159 bitop3:0x36
	v_bitop3_b32 v176, v171, s29, v170 bitop3:0x36
	s_or_b32 s29, s31, s30
	s_or_b32 s29, s29, 0xa0
	v_bitop3_b32 v175, v171, s29, v170 bitop3:0x36
	s_or_b32 s29, s2, 0xaa0
	s_xor_b32 s29, s29, 0x80
	v_xor_b32_e32 v174, s29, v154
	s_or_b32 s29, s26, 0x18e0
	v_bitop3_b32 v181, v171, s29, v170 bitop3:0x36
	s_or_b32 s29, s26, 0x1a60
	v_bitop3_b32 v177, v171, s29, v170 bitop3:0x36
	s_or_b32 s29, s31, 64
	s_or_b32 s3, s3, s29
	s_mov_b32 s41, s3
	s_or_b32 s29, s29, s33
	s_mov_b32 s40, s29
	s_or_b32 s3, s2, 0x18e0
	s_mov_b32 s42, s3
	s_or_b32 s2, s2, 0x1ae0
	s_xor_b32 s2, s2, 0x80
	s_mov_b32 s43, s2
	s_lshr_b32 s38, s4, 1
	v_and_b32_e32 v26, 31, v167
	v_and_b32_e32 v27, 3, v167
	v_bfe_u32 v28, v167, 3, 1
	v_bfe_u32 v29, v167, 2, 1
	v_lshl_or_b32 v27, v28, 2, v27
	v_lshl_or_b32 v27, v29, 3, v27
	v_lshlrev_b32_e32 v32, 9, v182
	v_lshl_add_u32 v30, v27, 3, v32
	v_add_u32_e32 v30, 0x10000, v30
	v_lshl_add_u32 v31, v26, 3, v32
	v_add_u32_e32 v31, 0x10400, v31
	v_xor_b32_e32 v28, 31, v26
	v_lshl_add_u32 v28, v28, 3, v32
	v_add_u32_e32 v28, 0x10400, v28
	v_bfe_u32 v29, v167, 4, 1
	v_mul_u32_u24_e32 v29, 0x78, v29
	v_xor_b32_e32 v254, s38, v29
	v_or_b32_e32 v254, 0x10800, v254
	v_and_b32_e32 v33, 16, v167
	v_cmp_eq_u32_e32 vcc, 0, v33
	ds_read2_b64 v[66:69], v30 offset0:0 offset1:32
	ds_read2_b64 v[70:73], v30 offset0:16 offset1:48
	ds_read2_b64 v[230:233], v31 offset0:0 offset1:32
	ds_read2_b64 v[234:237], v28 offset0:0 offset1:32
	ds_read2_b64 v[238:241], v254 offset0:0 offset1:16
	ds_read2_b64 v[242:245], v254 offset0:32 offset1:48
	s_waitcnt lgkmcnt(0)
	v_cndmask_b32_e32 v74, v67, v66, vcc
	v_cndmask_b32_e32 v75, v69, v68, vcc
	v_cndmask_b32_e64 v76, v66, -v67, vcc
	v_cndmask_b32_e64 v77, v68, -v69, vcc
	v_cndmask_b32_e32 v78, v71, v70, vcc
	v_cndmask_b32_e32 v79, v73, v72, vcc
	v_cndmask_b32_e64 v80, v70, -v71, vcc
	v_cndmask_b32_e64 v81, v72, -v73, vcc
	v_cvt_pk_f16_f32 v222, v74, v75
	v_cvt_pk_f16_f32 v223, v74, v75
	v_cvt_pk_f16_f32 v224, v76, v77
	v_cvt_pk_f16_f32 v225, v76, v77
	v_cvt_pk_f16_f32 v226, v78, v79
	v_cvt_pk_f16_f32 v227, v78, v79
	v_cvt_pk_f16_f32 v228, v80, v81
	v_cvt_pk_f16_f32 v229, v80, v81
	v_mul_f32_e32 v66, v231, v239
	v_mul_f32_e32 v68, v231, v238
	v_mul_f32_e32 v67, v231, v241
	v_mul_f32_e32 v69, v231, v240
	v_fma_f32 v66, v230, v238, -v66
	v_fma_f32 v68, v230, v239, v68
	v_fma_f32 v67, v230, v240, -v67
	v_fma_f32 v69, v230, v241, v69
	v_cvt_pk_f16_f32 v246, v66, v67
	v_cvt_pk_f16_f32 v248, v68, v69
	v_mul_f32_e32 v70, v233, v243
	v_mul_f32_e32 v72, v233, v242
	v_mul_f32_e32 v71, v233, v245
	v_mul_f32_e32 v73, v233, v244
	v_fma_f32 v70, v232, v242, -v70
	v_fma_f32 v72, v232, v243, v72
	v_fma_f32 v71, v232, v244, -v71
	v_fma_f32 v73, v232, v245, v73
	v_cvt_pk_f16_f32 v247, v70, v71
	v_cvt_pk_f16_f32 v249, v72, v73
	v_mul_f32_e32 v66, v235, v239
	v_mul_f32_e32 v68, v235, v238
	v_mul_f32_e32 v67, v235, v241
	v_mul_f32_e32 v69, v235, v240
	v_fma_f32 v66, v234, v238, -v66
	v_fma_f32 v68, v234, v239, v68
	v_fma_f32 v67, v234, v240, -v67
	v_fma_f32 v69, v234, v241, v69
	v_cvt_pk_f16_f32 v250, v66, v67
	v_cvt_pk_f16_f32 v252, v68, v69
	v_mul_f32_e32 v70, v237, v243
	v_mul_f32_e32 v72, v237, v242
	v_mul_f32_e32 v71, v237, v245
	v_mul_f32_e32 v73, v237, v244
	v_fma_f32 v70, v236, v242, -v70
	v_fma_f32 v72, v236, v243, v72
	v_fma_f32 v71, v236, v244, -v71
	v_fma_f32 v73, v236, v245, v73
	v_cvt_pk_f16_f32 v251, v70, v71
	v_cvt_pk_f16_f32 v253, v72, v73
	v_xor_b32_e32 v255, 8, v254
	ds_read2_b64 v[238:241], v255 offset0:0 offset1:16
	ds_read2_b64 v[242:245], v255 offset0:32 offset1:48
	v_mfma_f32_32x32x16_f16 v[2:17], v[222:225], v[246:249], 0
	v_mfma_f32_32x32x16_f16 v[18:33], v[226:229], v[250:253], 0
	s_waitcnt lgkmcnt(0)
	v_mul_f32_e32 v66, v231, v239
	v_mul_f32_e32 v68, v231, v238
	v_mul_f32_e32 v67, v231, v241
	v_mul_f32_e32 v69, v231, v240
	v_fma_f32 v66, v230, v238, -v66
	v_fma_f32 v68, v230, v239, v68
	v_fma_f32 v67, v230, v240, -v67
	v_fma_f32 v69, v230, v241, v69
	v_cvt_pk_f16_f32 v246, v66, v67
	v_cvt_pk_f16_f32 v248, v68, v69
	v_mul_f32_e32 v70, v233, v243
	v_mul_f32_e32 v72, v233, v242
	v_mul_f32_e32 v71, v233, v245
	v_mul_f32_e32 v73, v233, v244
	v_fma_f32 v70, v232, v242, -v70
	v_fma_f32 v72, v232, v243, v72
	v_fma_f32 v71, v232, v244, -v71
	v_fma_f32 v73, v232, v245, v73
	v_cvt_pk_f16_f32 v247, v70, v71
	v_cvt_pk_f16_f32 v249, v72, v73
	v_cvt_pk_f16_f32 v2, v2, v3
	v_cvt_pk_f16_f32 v3, v4, v5
	v_cvt_pk_f16_f32 v4, v6, v7
	v_cvt_pk_f16_f32 v5, v8, v9
	v_cvt_pk_f16_f32 v6, v10, v11
	v_cvt_pk_f16_f32 v7, v12, v13
	v_cvt_pk_f16_f32 v8, v14, v15
	v_cvt_pk_f16_f32 v9, v16, v17
	v_cvt_pk_f16_f32 v18, v18, v19
	v_cvt_pk_f16_f32 v19, v20, v21
	v_cvt_pk_f16_f32 v20, v22, v23
	v_cvt_pk_f16_f32 v21, v24, v25
	v_cvt_pk_f16_f32 v22, v26, v27
	v_cvt_pk_f16_f32 v23, v28, v29
	v_cvt_pk_f16_f32 v24, v30, v31
	v_cvt_pk_f16_f32 v25, v32, v33
	s_setprio 1
	s_waitcnt vmcnt(14)
	v_mul_f32_e32 v66, v235, v239
	v_mul_f32_e32 v68, v235, v238
	v_mfma_f32_32x32x16_f16 v[34:49], v[2:5], v[150:153], 0
	v_mul_f32_e32 v67, v235, v241
	v_mul_f32_e32 v69, v235, v240
	v_mfma_f32_32x32x16_f16 v[34:49], v[18:21], v[146:149], v[34:49]
	v_fma_f32 v66, v234, v238, -v66
	v_fma_f32 v68, v234, v239, v68
	v_mfma_f32_32x32x16_f16 v[34:49], v[6:9], v[142:145], v[34:49]
	v_fma_f32 v67, v234, v240, -v67
	v_fma_f32 v69, v234, v241, v69
	v_mfma_f32_32x32x16_f16 v[34:49], v[22:25], v[138:141], v[34:49]
	v_cvt_pk_f16_f32 v250, v66, v67
	v_cvt_pk_f16_f32 v252, v68, v69
	s_waitcnt vmcnt(5)
	v_mul_f32_e32 v70, v237, v243
	v_mul_f32_e32 v72, v237, v242
	v_mfma_f32_32x32x16_f16 v[50:65], v[2:5], v[134:137], 0
	v_mul_f32_e32 v71, v237, v245
	v_mul_f32_e32 v73, v237, v244
	v_mfma_f32_32x32x16_f16 v[50:65], v[18:21], v[126:129], v[50:65]
	v_fma_f32 v70, v236, v242, -v70
	v_fma_f32 v72, v236, v243, v72
	v_mfma_f32_32x32x16_f16 v[50:65], v[6:9], v[122:125], v[50:65]
	v_fma_f32 v71, v236, v244, -v71
	v_fma_f32 v73, v236, v245, v73
	v_mfma_f32_32x32x16_f16 v[50:65], v[22:25], v[130:133], v[50:65]
	v_cvt_pk_f16_f32 v251, v70, v71
	v_cvt_pk_f16_f32 v253, v72, v73
	v_xor_b32_e32 v255, 16, v254
	ds_read2_b64 v[238:241], v255 offset0:0 offset1:16
	ds_read2_b64 v[242:245], v255 offset0:32 offset1:48
	v_mfma_f32_32x32x16_f16 v[2:17], v[222:225], v[246:249], 0
	v_mfma_f32_32x32x16_f16 v[18:33], v[226:229], v[250:253], 0
	v_cvt_pk_f16_f32 v34, v34, v35
	v_cvt_pk_f16_f32 v35, v36, v37
	v_cvt_pk_f16_f32 v36, v38, v39
	v_cvt_pk_f16_f32 v37, v40, v41
	v_cvt_pk_f16_f32 v38, v42, v43
	v_cvt_pk_f16_f32 v39, v44, v45
	v_cvt_pk_f16_f32 v40, v46, v47
	v_cvt_pk_f16_f32 v41, v48, v49
	v_cvt_pk_f16_f32 v50, v50, v51
	v_cvt_pk_f16_f32 v51, v52, v53
	v_cvt_pk_f16_f32 v52, v54, v55
	v_cvt_pk_f16_f32 v53, v56, v57
	v_cvt_pk_f16_f32 v54, v58, v59
	v_cvt_pk_f16_f32 v55, v60, v61
	v_cvt_pk_f16_f32 v56, v62, v63
	v_cvt_pk_f16_f32 v57, v64, v65
	s_waitcnt vmcnt(2)
	v_cvt_pk_f16_f32 v2, v2, v3
	v_cvt_pk_f16_f32 v3, v4, v5
	v_cvt_pk_f16_f32 v4, v6, v7
	v_cvt_pk_f16_f32 v5, v8, v9
	v_mfma_f32_32x32x16_f16 v[190:205], v[34:37], v[118:121], 0
	v_cvt_pk_f16_f32 v6, v10, v11
	v_cvt_pk_f16_f32 v7, v12, v13
	v_cvt_pk_f16_f32 v8, v14, v15
	v_cvt_pk_f16_f32 v9, v16, v17
	v_mfma_f32_32x32x16_f16 v[206:221], v[34:37], v[102:105], 0
	v_cvt_pk_f16_f32 v18, v18, v19
	v_cvt_pk_f16_f32 v19, v20, v21
	v_cvt_pk_f16_f32 v20, v22, v23
	v_cvt_pk_f16_f32 v21, v24, v25
	v_mfma_f32_32x32x16_f16 v[190:205], v[38:41], v[114:117], v[190:205]
	v_cvt_pk_f16_f32 v22, v26, v27
	v_cvt_pk_f16_f32 v23, v28, v29
	v_cvt_pk_f16_f32 v24, v30, v31
	v_cvt_pk_f16_f32 v25, v32, v33
	v_mfma_f32_32x32x16_f16 v[206:221], v[38:41], v[98:101], v[206:221]
	s_waitcnt lgkmcnt(0)
	v_mul_f32_e32 v66, v231, v239
	v_mul_f32_e32 v68, v231, v238
	v_mul_f32_e32 v67, v231, v241
	v_mfma_f32_32x32x16_f16 v[190:205], v[50:53], v[110:113], v[190:205]
	v_mul_f32_e32 v69, v231, v240
	v_fma_f32 v66, v230, v238, -v66
	v_fma_f32 v68, v230, v239, v68
	v_fma_f32 v67, v230, v240, -v67
	v_mfma_f32_32x32x16_f16 v[206:221], v[50:53], v[94:97], v[206:221]
	v_fma_f32 v69, v230, v241, v69
	v_cvt_pk_f16_f32 v246, v66, v67
	v_cvt_pk_f16_f32 v248, v68, v69
	v_mul_f32_e32 v70, v233, v243
	v_mfma_f32_32x32x16_f16 v[190:205], v[54:57], v[106:109], v[190:205]
	v_mul_f32_e32 v72, v233, v242
	v_mul_f32_e32 v71, v233, v245
	v_mul_f32_e32 v73, v233, v244
	v_fma_f32 v70, v232, v242, -v70
	v_mfma_f32_32x32x16_f16 v[206:221], v[54:57], v[90:93], v[206:221]
	v_fma_f32 v72, v232, v243, v72
	v_fma_f32 v71, v232, v244, -v71
	v_fma_f32 v73, v232, v245, v73
	v_cvt_pk_f16_f32 v247, v70, v71
	v_cvt_pk_f16_f32 v249, v72, v73
	v_mfma_f32_32x32x16_f16 v[34:49], v[2:5], v[150:153], 0
	v_mul_f32_e32 v66, v235, v239
	v_mul_f32_e32 v68, v235, v238
	v_mul_f32_e32 v67, v235, v241
	v_mul_f32_e32 v69, v235, v240
	v_fma_f32 v66, v234, v238, -v66
	v_mfma_f32_32x32x16_f16 v[34:49], v[18:21], v[146:149], v[34:49]
	v_fma_f32 v68, v234, v239, v68
	v_fma_f32 v67, v234, v240, -v67
	v_fma_f32 v69, v234, v241, v69
	v_cvt_pk_f16_f32 v250, v66, v67
	v_cvt_pk_f16_f32 v252, v68, v69
	v_mfma_f32_32x32x16_f16 v[34:49], v[6:9], v[142:145], v[34:49]
	v_mul_f32_e32 v70, v237, v243
	v_mul_f32_e32 v72, v237, v242
	v_mul_f32_e32 v71, v237, v245
	v_mul_f32_e32 v73, v237, v244
	v_fma_f32 v70, v236, v242, -v70
	v_mfma_f32_32x32x16_f16 v[34:49], v[22:25], v[138:141], v[34:49]
	v_fma_f32 v72, v236, v243, v72
	v_fma_f32 v71, v236, v244, -v71
	v_fma_f32 v73, v236, v245, v73
	v_cvt_pk_f16_f32 v251, v70, v71
	v_cvt_pk_f16_f32 v253, v72, v73
	v_mfma_f32_32x32x16_f16 v[50:65], v[2:5], v[134:137], 0
	v_cvt_pk_f16_f32 v190, v190, v191
	v_cvt_pk_f16_f32 v191, v192, v193
	v_cvt_pk_f16_f32 v192, v194, v195
	v_cvt_pk_f16_f32 v193, v196, v197
	v_cvt_pk_f16_f32 v194, v198, v199
	v_mfma_f32_32x32x16_f16 v[50:65], v[18:21], v[126:129], v[50:65]
	v_cvt_pk_f16_f32 v195, v200, v201
	v_cvt_pk_f16_f32 v196, v202, v203
	v_cvt_pk_f16_f32 v197, v204, v205
	v_cvt_pk_f16_f32 v206, v206, v207
	v_cvt_pk_f16_f32 v207, v208, v209
	v_mfma_f32_32x32x16_f16 v[50:65], v[6:9], v[122:125], v[50:65]
	v_cvt_pk_f16_f32 v208, v210, v211
	v_cvt_pk_f16_f32 v209, v212, v213
	v_cvt_pk_f16_f32 v210, v214, v215
	v_cvt_pk_f16_f32 v211, v216, v217
	v_cvt_pk_f16_f32 v212, v218, v219
	v_mfma_f32_32x32x16_f16 v[50:65], v[22:25], v[130:133], v[50:65]
	v_cvt_pk_f16_f32 v213, v220, v221
	ds_write_b128 v173, v[190:193]
	ds_write_b128 v172, v[194:197]
	ds_write_b128 v173, v[206:209] offset:32768
	ds_write_b128 v172, v[210:213] offset:32768
	v_xor_b32_e32 v255, 24, v254
	ds_read2_b64 v[238:241], v255 offset0:0 offset1:16
	ds_read2_b64 v[242:245], v255 offset0:32 offset1:48
	v_mfma_f32_32x32x16_f16 v[2:17], v[222:225], v[246:249], 0
	v_mfma_f32_32x32x16_f16 v[18:33], v[226:229], v[250:253], 0
	v_cvt_pk_f16_f32 v34, v34, v35
	v_cvt_pk_f16_f32 v35, v36, v37
	v_cvt_pk_f16_f32 v36, v38, v39
	v_cvt_pk_f16_f32 v37, v40, v41
	v_cvt_pk_f16_f32 v38, v42, v43
	v_cvt_pk_f16_f32 v39, v44, v45
	v_cvt_pk_f16_f32 v40, v46, v47
	v_cvt_pk_f16_f32 v41, v48, v49
	v_cvt_pk_f16_f32 v50, v50, v51
	v_cvt_pk_f16_f32 v51, v52, v53
	v_cvt_pk_f16_f32 v52, v54, v55
	v_cvt_pk_f16_f32 v53, v56, v57
	v_cvt_pk_f16_f32 v54, v58, v59
	v_cvt_pk_f16_f32 v55, v60, v61
	v_cvt_pk_f16_f32 v56, v62, v63
	v_cvt_pk_f16_f32 v57, v64, v65
	v_mfma_f32_32x32x16_f16 v[190:205], v[34:37], v[118:121], 0
	v_cvt_pk_f16_f32 v2, v2, v3
	v_cvt_pk_f16_f32 v3, v4, v5
	v_cvt_pk_f16_f32 v4, v6, v7
	v_cvt_pk_f16_f32 v5, v8, v9
	v_mfma_f32_32x32x16_f16 v[206:221], v[34:37], v[102:105], 0
	v_cvt_pk_f16_f32 v6, v10, v11
	v_cvt_pk_f16_f32 v7, v12, v13
	v_cvt_pk_f16_f32 v8, v14, v15
	v_cvt_pk_f16_f32 v9, v16, v17
	v_cvt_pk_f16_f32 v18, v18, v19
	v_mfma_f32_32x32x16_f16 v[190:205], v[38:41], v[114:117], v[190:205]
	v_cvt_pk_f16_f32 v19, v20, v21
	v_cvt_pk_f16_f32 v20, v22, v23
	v_cvt_pk_f16_f32 v21, v24, v25
	v_cvt_pk_f16_f32 v22, v26, v27
	v_mfma_f32_32x32x16_f16 v[206:221], v[38:41], v[98:101], v[206:221]
	v_cvt_pk_f16_f32 v23, v28, v29
	v_cvt_pk_f16_f32 v24, v30, v31
	v_cvt_pk_f16_f32 v25, v32, v33
	s_waitcnt lgkmcnt(0)
	v_mul_f32_e32 v66, v231, v239
	v_mfma_f32_32x32x16_f16 v[190:205], v[50:53], v[110:113], v[190:205]
	v_mul_f32_e32 v68, v231, v238
	v_mul_f32_e32 v67, v231, v241
	v_mul_f32_e32 v69, v231, v240
	v_fma_f32 v66, v230, v238, -v66
	v_fma_f32 v68, v230, v239, v68
	v_mfma_f32_32x32x16_f16 v[206:221], v[50:53], v[94:97], v[206:221]
	v_fma_f32 v67, v230, v240, -v67
	v_fma_f32 v69, v230, v241, v69
	v_cvt_pk_f16_f32 v246, v66, v67
	v_cvt_pk_f16_f32 v248, v68, v69
	v_mfma_f32_32x32x16_f16 v[190:205], v[54:57], v[106:109], v[190:205]
	v_mul_f32_e32 v70, v233, v243
	v_mul_f32_e32 v72, v233, v242
	v_mul_f32_e32 v71, v233, v245
	v_mul_f32_e32 v73, v233, v244
	v_fma_f32 v70, v232, v242, -v70
	v_mfma_f32_32x32x16_f16 v[206:221], v[54:57], v[90:93], v[206:221]
	v_fma_f32 v72, v232, v243, v72
	v_fma_f32 v71, v232, v244, -v71
	v_fma_f32 v73, v232, v245, v73
	v_cvt_pk_f16_f32 v247, v70, v71
	v_cvt_pk_f16_f32 v249, v72, v73
	v_mfma_f32_32x32x16_f16 v[34:49], v[2:5], v[150:153], 0
	v_mul_f32_e32 v66, v235, v239
	v_mul_f32_e32 v68, v235, v238
	v_mul_f32_e32 v67, v235, v241
	v_mul_f32_e32 v69, v235, v240
	v_fma_f32 v66, v234, v238, -v66
	v_mfma_f32_32x32x16_f16 v[34:49], v[18:21], v[146:149], v[34:49]
	v_fma_f32 v68, v234, v239, v68
	v_fma_f32 v67, v234, v240, -v67
	v_fma_f32 v69, v234, v241, v69
	v_cvt_pk_f16_f32 v250, v66, v67
	v_cvt_pk_f16_f32 v252, v68, v69
	v_mfma_f32_32x32x16_f16 v[34:49], v[6:9], v[142:145], v[34:49]
	v_mul_f32_e32 v70, v237, v243
	v_mul_f32_e32 v72, v237, v242
	v_mul_f32_e32 v71, v237, v245
	v_mul_f32_e32 v73, v237, v244
	v_fma_f32 v70, v236, v242, -v70
	v_mfma_f32_32x32x16_f16 v[34:49], v[22:25], v[138:141], v[34:49]
	v_fma_f32 v72, v236, v243, v72
	v_fma_f32 v71, v236, v244, -v71
	v_fma_f32 v73, v236, v245, v73
	v_cvt_pk_f16_f32 v251, v70, v71
	v_cvt_pk_f16_f32 v253, v72, v73
	v_cvt_pk_f16_f32 v190, v190, v191
	v_mfma_f32_32x32x16_f16 v[50:65], v[2:5], v[134:137], 0
	v_cvt_pk_f16_f32 v191, v192, v193
	v_cvt_pk_f16_f32 v192, v194, v195
	v_cvt_pk_f16_f32 v193, v196, v197
	v_cvt_pk_f16_f32 v194, v198, v199
	v_cvt_pk_f16_f32 v195, v200, v201
	v_mfma_f32_32x32x16_f16 v[50:65], v[18:21], v[126:129], v[50:65]
	v_cvt_pk_f16_f32 v196, v202, v203
	v_cvt_pk_f16_f32 v197, v204, v205
	v_cvt_pk_f16_f32 v206, v206, v207
	v_cvt_pk_f16_f32 v207, v208, v209
	v_cvt_pk_f16_f32 v208, v210, v211
	v_mfma_f32_32x32x16_f16 v[50:65], v[6:9], v[122:125], v[50:65]
	v_cvt_pk_f16_f32 v209, v212, v213
	v_cvt_pk_f16_f32 v210, v214, v215
	v_cvt_pk_f16_f32 v211, v216, v217
	v_cvt_pk_f16_f32 v212, v218, v219
	v_cvt_pk_f16_f32 v213, v220, v221
	v_mfma_f32_32x32x16_f16 v[50:65], v[22:25], v[130:133], v[50:65]
	v_xor_b32_e32 v74, 0x8a0, v173
	v_xor_b32_e32 v75, 0x8a0, v172
	ds_write_b128 v74, v[190:193]
	ds_write_b128 v75, v[194:197]
	ds_write_b128 v74, v[206:209] offset:32768
	ds_write_b128 v75, v[210:213] offset:32768
	s_nop 0
	v_mfma_f32_32x32x16_f16 v[2:17], v[222:225], v[246:249], 0
	v_mfma_f32_32x32x16_f16 v[18:33], v[226:229], v[250:253], 0
	v_cvt_pk_f16_f32 v34, v34, v35
	v_cvt_pk_f16_f32 v35, v36, v37
	v_cvt_pk_f16_f32 v36, v38, v39
	v_cvt_pk_f16_f32 v37, v40, v41
	v_cvt_pk_f16_f32 v38, v42, v43
	v_cvt_pk_f16_f32 v39, v44, v45
	v_cvt_pk_f16_f32 v40, v46, v47
	v_cvt_pk_f16_f32 v41, v48, v49
	v_cvt_pk_f16_f32 v50, v50, v51
	v_cvt_pk_f16_f32 v51, v52, v53
	v_cvt_pk_f16_f32 v52, v54, v55
	v_cvt_pk_f16_f32 v53, v56, v57
	v_cvt_pk_f16_f32 v54, v58, v59
	v_cvt_pk_f16_f32 v55, v60, v61
	v_cvt_pk_f16_f32 v56, v62, v63
	v_cvt_pk_f16_f32 v57, v64, v65
	v_mfma_f32_32x32x16_f16 v[190:205], v[34:37], v[118:121], 0
	v_cvt_pk_f16_f32 v2, v2, v3
	v_cvt_pk_f16_f32 v3, v4, v5
	v_mfma_f32_32x32x16_f16 v[206:221], v[34:37], v[102:105], 0
	v_cvt_pk_f16_f32 v4, v6, v7
	v_cvt_pk_f16_f32 v5, v8, v9
	v_mfma_f32_32x32x16_f16 v[190:205], v[38:41], v[114:117], v[190:205]
	v_cvt_pk_f16_f32 v6, v10, v11
	v_cvt_pk_f16_f32 v7, v12, v13
	v_mfma_f32_32x32x16_f16 v[206:221], v[38:41], v[98:101], v[206:221]
	v_cvt_pk_f16_f32 v8, v14, v15
	v_cvt_pk_f16_f32 v9, v16, v17
	v_mfma_f32_32x32x16_f16 v[190:205], v[50:53], v[110:113], v[190:205]
	v_cvt_pk_f16_f32 v18, v18, v19
	v_cvt_pk_f16_f32 v19, v20, v21
	v_mfma_f32_32x32x16_f16 v[206:221], v[50:53], v[94:97], v[206:221]
	v_cvt_pk_f16_f32 v20, v22, v23
	v_cvt_pk_f16_f32 v21, v24, v25
	v_mfma_f32_32x32x16_f16 v[190:205], v[54:57], v[106:109], v[190:205]
	v_cvt_pk_f16_f32 v22, v26, v27
	v_cvt_pk_f16_f32 v23, v28, v29
	v_mfma_f32_32x32x16_f16 v[206:221], v[54:57], v[90:93], v[206:221]
	v_cvt_pk_f16_f32 v24, v30, v31
	v_cvt_pk_f16_f32 v25, v32, v33
	v_mfma_f32_32x32x16_f16 v[34:49], v[2:5], v[150:153], 0
	v_mfma_f32_32x32x16_f16 v[34:49], v[18:21], v[146:149], v[34:49]
	v_mfma_f32_32x32x16_f16 v[34:49], v[6:9], v[142:145], v[34:49]
	v_mfma_f32_32x32x16_f16 v[34:49], v[22:25], v[138:141], v[34:49]
	v_mfma_f32_32x32x16_f16 v[50:65], v[2:5], v[134:137], 0
	s_nop 5
	v_cvt_pk_f16_f32 v190, v190, v191
	v_cvt_pk_f16_f32 v191, v192, v193
	v_cvt_pk_f16_f32 v192, v194, v195
	v_cvt_pk_f16_f32 v193, v196, v197
	v_mfma_f32_32x32x16_f16 v[50:65], v[18:21], v[126:129], v[50:65]
	v_cvt_pk_f16_f32 v194, v198, v199
	v_cvt_pk_f16_f32 v195, v200, v201
	v_cvt_pk_f16_f32 v196, v202, v203
	v_cvt_pk_f16_f32 v197, v204, v205
	v_cvt_pk_f16_f32 v206, v206, v207
	v_cvt_pk_f16_f32 v207, v208, v209
	v_mfma_f32_32x32x16_f16 v[50:65], v[6:9], v[122:125], v[50:65]
	v_cvt_pk_f16_f32 v208, v210, v211
	v_cvt_pk_f16_f32 v209, v212, v213
	v_cvt_pk_f16_f32 v210, v214, v215
	v_cvt_pk_f16_f32 v211, v216, v217
	v_cvt_pk_f16_f32 v212, v218, v219
	v_cvt_pk_f16_f32 v213, v220, v221
	v_mfma_f32_32x32x16_f16 v[50:65], v[22:25], v[130:133], v[50:65]
	v_xor_b32_e32 v74, 0x1040, v173
	v_xor_b32_e32 v75, 0x1040, v172
	ds_write_b128 v74, v[190:193]
	ds_write_b128 v75, v[194:197]
	ds_write_b128 v74, v[206:209] offset:32768
	ds_write_b128 v75, v[210:213] offset:32768
	s_nop 11
	v_cvt_pk_f16_f32 v34, v34, v35
	v_cvt_pk_f16_f32 v35, v36, v37
	v_cvt_pk_f16_f32 v36, v38, v39
	v_cvt_pk_f16_f32 v37, v40, v41
	v_cvt_pk_f16_f32 v38, v42, v43
	v_cvt_pk_f16_f32 v39, v44, v45
	v_cvt_pk_f16_f32 v40, v46, v47
	v_cvt_pk_f16_f32 v41, v48, v49
	v_cvt_pk_f16_f32 v50, v50, v51
	v_cvt_pk_f16_f32 v51, v52, v53
	v_cvt_pk_f16_f32 v52, v54, v55
	v_cvt_pk_f16_f32 v53, v56, v57
	v_cvt_pk_f16_f32 v54, v58, v59
	v_cvt_pk_f16_f32 v55, v60, v61
	v_cvt_pk_f16_f32 v56, v62, v63
	v_cvt_pk_f16_f32 v57, v64, v65
	v_mfma_f32_32x32x16_f16 v[190:205], v[34:37], v[118:121], 0
	v_mfma_f32_32x32x16_f16 v[206:221], v[34:37], v[102:105], 0
	v_mfma_f32_32x32x16_f16 v[190:205], v[38:41], v[114:117], v[190:205]
	v_mfma_f32_32x32x16_f16 v[206:221], v[38:41], v[98:101], v[206:221]
	v_mfma_f32_32x32x16_f16 v[190:205], v[50:53], v[110:113], v[190:205]
	v_mfma_f32_32x32x16_f16 v[206:221], v[50:53], v[94:97], v[206:221]
	v_mfma_f32_32x32x16_f16 v[190:205], v[54:57], v[106:109], v[190:205]
	v_mfma_f32_32x32x16_f16 v[206:221], v[54:57], v[90:93], v[206:221]
	v_and_b32_e32 v134, 1, v156
	v_bitop3_b32 v132, v171, s40, v170 bitop3:0x36
	v_bitop3_b32 v131, s41, v154, v160 bitop3:0x36
	v_bitop3_b32 v135, v171, s42, v170 bitop3:0x36
	v_xor_b32_e32 v133, s43, v154
	v_and_b32_e32 v130, 4, v156
	s_lshl_b32 s2, s27, 3
	s_lshl_b32 s3, s5, 2
	s_or_b32 s2, s3, s2
	s_ashr_i32 s3, s2, 31
	s_lshl_b64 s[2:3], s[2:3], 13
	s_add_u32 s2, s20, s2
	s_addc_u32 s3, s21, s3
	v_lshlrev_b32_e32 v154, 1, v169
	v_lshl_add_u64 v[2:3], s[2:3], 0, v[154:155]
	v_add_co_u32_e32 v2, vcc, s23, v2
	s_nop 1
	v_addc_co_u32_e32 v3, vcc, 0, v3, vcc
	v_cvt_pk_f16_f32 v190, v190, v191
	v_cvt_pk_f16_f32 v191, v192, v193
	v_cvt_pk_f16_f32 v192, v194, v195
	v_cvt_pk_f16_f32 v193, v196, v197
	v_cvt_pk_f16_f32 v194, v198, v199
	v_cvt_pk_f16_f32 v195, v200, v201
	v_cvt_pk_f16_f32 v196, v202, v203
	v_cvt_pk_f16_f32 v197, v204, v205
	v_cvt_pk_f16_f32 v206, v206, v207
	v_cvt_pk_f16_f32 v207, v208, v209
	v_cvt_pk_f16_f32 v208, v210, v211
	v_cvt_pk_f16_f32 v209, v212, v213
	v_cvt_pk_f16_f32 v210, v214, v215
	v_cvt_pk_f16_f32 v211, v216, v217
	v_cvt_pk_f16_f32 v212, v218, v219
	v_cvt_pk_f16_f32 v213, v220, v221
	v_xor_b32_e32 v74, 0x18e0, v173
	v_xor_b32_e32 v75, 0x18e0, v172
	ds_write_b128 v74, v[190:193]
	ds_write_b128 v75, v[194:197]
	ds_write_b128 v74, v[206:209] offset:32768
	ds_write_b128 v75, v[210:213] offset:32768
	s_setprio 0
	s_waitcnt lgkmcnt(0)
	s_barrier
	global_load_dwordx4 v[62:65], v154, s[2:3]
	global_load_dwordx4 v[46:49], v154, s[2:3] offset:1024
	global_load_dwordx4 v[42:45], v154, s[2:3] offset:2048
	global_load_dwordx4 v[38:41], v154, s[2:3] offset:3072
	global_load_dwordx4 v[54:57], v[2:3], off offset:1024
	global_load_dwordx4 v[50:53], v[2:3], off offset:2048
	v_lshl_add_u64 v[4:5], s[12:13], 0, v[154:155]
	global_load_dwordx4 v[126:129], v154, s[12:13]
	global_load_dwordx4 v[122:125], v154, s[12:13] offset:1024
	global_load_dwordx4 v[118:121], v154, s[12:13] offset:2048
	global_load_dwordx4 v[114:117], v154, s[12:13] offset:3072
	global_load_dwordx4 v[34:37], v168, s[2:3]
	global_load_dwordx4 v[110:113], v168, s[12:13]
	v_add_co_u32_e32 v4, vcc, s23, v4
	s_nop 1
	v_addc_co_u32_e32 v5, vcc, 0, v5, vcc
	global_load_dwordx4 v[58:61], v[2:3], off offset:3072
	global_load_dwordx4 v[106:109], v[4:5], off offset:1024
	global_load_dwordx4 v[94:97], v[4:5], off offset:2048
	global_load_dwordx4 v[90:93], v[4:5], off offset:3072
	v_bfrev_b32_e32 v3, v156
	v_lshlrev_b32_e32 v7, 5, v167
	v_lshlrev_b32_e32 v6, 9, v167
	v_and_b32_e32 v7, 0x200, v7
	v_lshlrev_b32_e32 v8, 8, v167
	v_lshrrev_b32_e32 v3, 27, v3
	v_lshrrev_b32_e32 v2, 2, v167
	v_lshrrev_b32_e32 v4, 4, v156
	v_xor_b32_e32 v5, v169, v156
	v_and_b32_e32 v6, 0x5800, v6
	v_and_b32_e32 v3, 8, v3
	v_and_or_b32 v7, v8, s24, v7
	v_lshrrev_b32_e32 v5, 1, v5
	v_xor_b32_e32 v4, v2, v4
	v_or3_b32 v3, v7, v6, v3
	v_bitop3_b32 v7, v2, v182, 1 bitop3:0x6c
	v_lshlrev_b32_e32 v2, 1, v167
	v_and_b32_e32 v5, 4, v5
	v_lshlrev_b32_e32 v4, 3, v4
	v_lshrrev_b32_e32 v6, 1, v167
	v_and_b32_e32 v2, 2, v2
	v_and_or_b32 v9, v169, 8, v2
	v_and_b32_e32 v2, 8, v4
	v_and_or_b32 v4, v6, 2, v5
	v_or3_b32 v2, v4, v2, v134
	v_lshlrev_b32_e32 v2, 4, v2
	v_bitop3_b32 v146, v3, s28, v2 bitop3:0x36
	v_xor_b32_e32 v8, v6, v182
	v_xor_b32_e32 v147, 0x2010, v146
	v_lshlrev_b32_e32 v8, 2, v8
	v_and_b32_e32 v8, 4, v8
	v_or3_b32 v6, v9, v7, v8
	v_lshlrev_b32_e32 v7, 11, v167
	v_and_b32_e32 v8, 0x7800, v7
	v_lshlrev_b32_e32 v6, 4, v6
	v_or3_b32 v22, v6, v8, v170
	v_and_b32_e32 v23, 0x8000, v7
	v_xor_b32_e32 v150, 16, v146
	v_xad_u32 v70, v22, s28, v23
	v_xor_b32_e32 v151, 0x2000, v146
	ds_read_b64_tr_b16 v[18:19], v146
	ds_read_b64_tr_b16 v[20:21], v147
	ds_read_b64_tr_b16 v[22:23], v146 offset:32768
	ds_read_b64_tr_b16 v[24:25], v147 offset:32768
	ds_read_b64_tr_b16 v[26:27], v150
	ds_read_b64_tr_b16 v[28:29], v151
	ds_read_b64_tr_b16 v[30:31], v150 offset:32768
	ds_read_b64_tr_b16 v[32:33], v151 offset:32768
	v_xor_b32_e32 v148, 32, v146
	v_xor_b32_e32 v149, 0x2030, v146
	v_xor_b32_e32 v144, 48, v146
	v_xor_b32_e32 v145, 0x2020, v146
	v_xor_b32_e32 v142, 64, v146
	v_xor_b32_e32 v143, 0x2050, v146
	v_xor_b32_e32 v140, 0x50, v146
	v_xor_b32_e32 v141, 0x2040, v146
	v_xor_b32_e32 v138, 0x60, v146
	v_xor_b32_e32 v139, 0x2070, v146
	v_xor_b32_e32 v136, 0x70, v146
	v_xor_b32_e32 v137, 0x2060, v146
	v_xor_b32_e32 v71, 0x60, v70
	s_lshl_b64 s[0:1], s[0:1], 13
	s_add_u32 s0, s8, s0
	s_addc_u32 s1, s9, s1
	s_waitcnt vmcnt(17) lgkmcnt(4)
	v_mfma_f32_32x32x16_f16 v[2:17], v[18:21], v[86:89], 0
	s_waitcnt vmcnt(16)
	v_mfma_f32_32x32x16_f16 v[2:17], v[22:25], v[82:85], v[2:17]
	ds_read_b64_tr_b16 v[206:207], v148
	ds_read_b64_tr_b16 v[208:209], v149
	ds_read_b64_tr_b16 v[210:211], v148 offset:32768
	ds_read_b64_tr_b16 v[212:213], v149 offset:32768
	s_waitcnt lgkmcnt(4)
	v_mfma_f32_32x32x16_f16 v[190:205], v[26:29], v[86:89], 0
	v_mfma_f32_32x32x16_f16 v[190:205], v[30:33], v[82:85], v[190:205]
	s_nop 4
	v_cvt_pk_f16_f32 v2, v2, v3
	v_cvt_pk_f16_f32 v3, v4, v5
	v_cvt_pk_f16_f32 v4, v6, v7
	v_cvt_pk_f16_f32 v5, v8, v9
	v_cvt_pk_f16_f32 v6, v10, v11
	v_cvt_pk_f16_f32 v7, v12, v13
	v_cvt_pk_f16_f32 v8, v14, v15
	v_cvt_pk_f16_f32 v9, v16, v17
	v_xor_b32_e32 v73, 0x280, v70
	ds_write_b128 v70, v[2:5]
	ds_write_b128 v73, v[6:9]
	ds_read_b64_tr_b16 v[18:19], v144
	ds_read_b64_tr_b16 v[20:21], v145
	ds_read_b64_tr_b16 v[22:23], v144 offset:32768
	ds_read_b64_tr_b16 v[24:25], v145 offset:32768
	s_waitcnt lgkmcnt(6)
	v_mfma_f32_32x32x16_f16 v[2:17], v[206:209], v[86:89], 0
	v_mfma_f32_32x32x16_f16 v[2:17], v[210:213], v[82:85], v[2:17]
	v_cvt_pk_f16_f32 v190, v190, v191
	v_cvt_pk_f16_f32 v191, v192, v193
	v_cvt_pk_f16_f32 v192, v194, v195
	v_cvt_pk_f16_f32 v193, v196, v197
	v_cvt_pk_f16_f32 v194, v198, v199
	v_cvt_pk_f16_f32 v195, v200, v201
	v_cvt_pk_f16_f32 v196, v202, v203
	v_cvt_pk_f16_f32 v197, v204, v205
	v_xor_b32_e32 v72, 16, v70
	v_xor_b32_e32 v73, 0x290, v70
	ds_write_b128 v72, v[190:193]
	ds_write_b128 v73, v[194:197]
	ds_read_b64_tr_b16 v[26:27], v142
	ds_read_b64_tr_b16 v[28:29], v143
	ds_read_b64_tr_b16 v[30:31], v142 offset:32768
	ds_read_b64_tr_b16 v[32:33], v143 offset:32768
	s_waitcnt lgkmcnt(6)
	v_mfma_f32_32x32x16_f16 v[190:205], v[18:21], v[86:89], 0
	v_mfma_f32_32x32x16_f16 v[190:205], v[22:25], v[82:85], v[190:205]
	v_cvt_pk_f16_f32 v2, v2, v3
	v_cvt_pk_f16_f32 v3, v4, v5
	v_cvt_pk_f16_f32 v4, v6, v7
	v_cvt_pk_f16_f32 v5, v8, v9
	v_cvt_pk_f16_f32 v6, v10, v11
	v_cvt_pk_f16_f32 v7, v12, v13
	v_cvt_pk_f16_f32 v8, v14, v15
	v_cvt_pk_f16_f32 v9, v16, v17
	v_xor_b32_e32 v72, 32, v70
	v_xor_b32_e32 v73, 0x2a0, v70
	ds_write_b128 v72, v[2:5]
	ds_write_b128 v73, v[6:9]
	ds_read_b64_tr_b16 v[206:207], v140
	ds_read_b64_tr_b16 v[208:209], v141
	ds_read_b64_tr_b16 v[210:211], v140 offset:32768
	ds_read_b64_tr_b16 v[212:213], v141 offset:32768
	s_waitcnt lgkmcnt(6)
	v_mfma_f32_32x32x16_f16 v[2:17], v[26:29], v[86:89], 0
	v_mfma_f32_32x32x16_f16 v[2:17], v[30:33], v[82:85], v[2:17]
	v_cvt_pk_f16_f32 v190, v190, v191
	v_cvt_pk_f16_f32 v191, v192, v193
	v_cvt_pk_f16_f32 v192, v194, v195
	v_cvt_pk_f16_f32 v193, v196, v197
	v_cvt_pk_f16_f32 v194, v198, v199
	v_cvt_pk_f16_f32 v195, v200, v201
	v_cvt_pk_f16_f32 v196, v202, v203
	v_cvt_pk_f16_f32 v197, v204, v205
	v_xor_b32_e32 v72, 48, v70
	v_xor_b32_e32 v73, 0x2b0, v70
	ds_write_b128 v72, v[190:193]
	ds_write_b128 v73, v[194:197]
	ds_read_b64_tr_b16 v[18:19], v138
	ds_read_b64_tr_b16 v[20:21], v139
	ds_read_b64_tr_b16 v[22:23], v138 offset:32768
	ds_read_b64_tr_b16 v[24:25], v139 offset:32768
	s_waitcnt lgkmcnt(6)
	v_mfma_f32_32x32x16_f16 v[190:205], v[206:209], v[86:89], 0
	v_mfma_f32_32x32x16_f16 v[190:205], v[210:213], v[82:85], v[190:205]
	v_cvt_pk_f16_f32 v2, v2, v3
	v_cvt_pk_f16_f32 v3, v4, v5
	v_cvt_pk_f16_f32 v4, v6, v7
	v_cvt_pk_f16_f32 v5, v8, v9
	v_cvt_pk_f16_f32 v6, v10, v11
	v_cvt_pk_f16_f32 v7, v12, v13
	v_cvt_pk_f16_f32 v8, v14, v15
	v_cvt_pk_f16_f32 v9, v16, v17
	v_xor_b32_e32 v72, 64, v70
	v_xor_b32_e32 v73, 0x2c0, v70
	ds_write_b128 v72, v[2:5]
	ds_write_b128 v73, v[6:9]
	ds_read_b64_tr_b16 v[26:27], v136
	ds_read_b64_tr_b16 v[28:29], v137
	ds_read_b64_tr_b16 v[30:31], v136 offset:32768
	ds_read_b64_tr_b16 v[32:33], v137 offset:32768
	s_waitcnt lgkmcnt(6)
	v_mfma_f32_32x32x16_f16 v[2:17], v[18:21], v[86:89], 0
	v_mfma_f32_32x32x16_f16 v[2:17], v[22:25], v[82:85], v[2:17]
	v_cvt_pk_f16_f32 v190, v190, v191
	v_cvt_pk_f16_f32 v191, v192, v193
	v_cvt_pk_f16_f32 v192, v194, v195
	v_cvt_pk_f16_f32 v193, v196, v197
	v_cvt_pk_f16_f32 v194, v198, v199
	v_cvt_pk_f16_f32 v195, v200, v201
	v_cvt_pk_f16_f32 v196, v202, v203
	v_cvt_pk_f16_f32 v197, v204, v205
	v_xor_b32_e32 v72, 0x50, v70
	v_xor_b32_e32 v73, 0x2d0, v70
	ds_write_b128 v72, v[190:193]
	ds_write_b128 v73, v[194:197]
	s_waitcnt lgkmcnt(2)
	v_mfma_f32_32x32x16_f16 v[190:205], v[26:29], v[86:89], 0
	v_mfma_f32_32x32x16_f16 v[190:205], v[30:33], v[82:85], v[190:205]
	v_cvt_pk_f16_f32 v2, v2, v3
	v_cvt_pk_f16_f32 v3, v4, v5
	v_cvt_pk_f16_f32 v4, v6, v7
	v_cvt_pk_f16_f32 v5, v8, v9
	v_cvt_pk_f16_f32 v6, v10, v11
	v_cvt_pk_f16_f32 v7, v12, v13
	v_cvt_pk_f16_f32 v8, v14, v15
	v_cvt_pk_f16_f32 v9, v16, v17
	v_xor_b32_e32 v72, 0x60, v70
	v_xor_b32_e32 v73, 0x2e0, v70
	ds_write_b128 v72, v[2:5]
	ds_write_b128 v73, v[6:9]
	v_cvt_pk_f16_f32 v190, v190, v191
	v_cvt_pk_f16_f32 v191, v192, v193
	v_cvt_pk_f16_f32 v192, v194, v195
	v_cvt_pk_f16_f32 v193, v196, v197
	v_cvt_pk_f16_f32 v194, v198, v199
	v_cvt_pk_f16_f32 v195, v200, v201
	v_cvt_pk_f16_f32 v196, v202, v203
	v_cvt_pk_f16_f32 v197, v204, v205
	v_xor_b32_e32 v72, 0x70, v70
	v_xor_b32_e32 v73, 0x2f0, v70
	ds_write_b128 v72, v[190:193]
	ds_write_b128 v73, v[194:197]
	v_lshl_add_u64 v[2:3], s[0:1], 0, v[154:155]
	v_lshl_add_u64 v[4:5], v[2:3], 0, s[18:19]
	v_add_co_u32_e32 v2, vcc, s25, v2
	s_waitcnt lgkmcnt(0)
	s_nop 0
	v_addc_co_u32_e32 v3, vcc, 0, v3, vcc
	s_barrier
	global_load_dwordx4 v[102:105], v[2:3], off
	global_load_dwordx4 v[98:101], v[4:5], off offset:1024
	s_setprio 1
	s_add_u32 s0, s2, 0x2000
	s_addc_u32 s1, s3, 0
	v_lshl_add_u64 v[2:3], s[0:1], 0, v[154:155]
	v_add_co_u32_e32 v2, vcc, s23, v2
	global_load_dwordx4 v[66:69], v154, s[0:1]
	global_load_dwordx4 v[70:73], v154, s[0:1] offset:1024
	global_load_dwordx4 v[74:77], v154, s[0:1] offset:2048
	global_load_dwordx4 v[78:81], v154, s[0:1] offset:3072
	v_addc_co_u32_e32 v3, vcc, 0, v3, vcc
	global_load_dwordx4 v[82:85], v168, s[0:1]
	global_load_dwordx4 v[86:89], v[2:3], off offset:1024
	global_load_dwordx4 v[182:185], v[2:3], off offset:2048
	global_load_dwordx4 v[186:189], v[2:3], off offset:3072
	ds_read_b128 v[18:21], v179
	ds_read_b128 v[22:25], v179 offset:32768
	ds_read_b128 v[26:29], v178
	ds_read_b128 v[30:33], v178 offset:32768
	s_add_u32 s0, s2, 0x6000
	s_addc_u32 s1, s3, 0
	s_waitcnt vmcnt(25) lgkmcnt(3)
	v_mfma_f32_32x32x16_f16 v[2:17], v[18:21], v[62:65], 0
	s_add_u32 s2, s2, 0x4000
	s_addc_u32 s3, s3, 0
	s_or_b32 s27, s26, 0x8a0
	s_or_b32 s26, s26, 0xa20
	s_waitcnt vmcnt(24) lgkmcnt(1)
	v_mfma_f32_32x32x16_f16 v[2:17], v[26:29], v[46:49], v[2:17]
	s_waitcnt vmcnt(23)
	v_mfma_f32_32x32x16_f16 v[2:17], v[22:25], v[42:45], v[2:17]
	s_waitcnt vmcnt(22) lgkmcnt(0)
	v_mfma_f32_32x32x16_f16 v[2:17], v[30:33], v[38:41], v[2:17]
	s_waitcnt vmcnt(15)
	v_mfma_f32_32x32x16_f16 v[34:49], v[18:21], v[34:37], 0
	s_nop 9
	v_cvt_pk_f16_f32 v9, v8, v9
	v_cvt_pk_f16_f32 v8, v6, v7
	v_cvt_pk_f16_f32 v7, v4, v5
	v_cvt_pk_f16_f32 v6, v2, v3
	v_cvt_pk_f16_f32 v5, v16, v17
	v_cvt_pk_f16_f32 v4, v14, v15
	v_cvt_pk_f16_f32 v3, v12, v13
	v_mfma_f32_32x32x16_f16 v[34:49], v[26:29], v[54:57], v[34:49]
	v_cvt_pk_f16_f32 v2, v10, v11
	v_mfma_f32_32x32x16_f16 v[34:49], v[22:25], v[50:53], v[34:49]
	s_waitcnt vmcnt(13)
	v_mfma_f32_32x32x16_f16 v[34:49], v[30:33], v[58:61], v[34:49]
	v_mfma_f32_32x32x16_f16 v[18:33], v[6:9], v[126:129], 0
	s_nop 10
	v_cvt_pk_f16_f32 v13, v40, v41
	v_cvt_pk_f16_f32 v12, v38, v39
	v_cvt_pk_f16_f32 v11, v36, v37
	v_cvt_pk_f16_f32 v10, v34, v35
	v_cvt_pk_f16_f32 v17, v48, v49
	v_cvt_pk_f16_f32 v16, v46, v47
	v_cvt_pk_f16_f32 v15, v44, v45
	v_mfma_f32_32x32x16_f16 v[50:65], v[6:9], v[110:113], 0
	v_bitop3_b32 v6, v171, s27, v170 bitop3:0x36
	v_cvt_pk_f16_f32 v14, v42, v43
	v_mfma_f32_32x32x16_f16 v[18:33], v[2:5], v[122:125], v[18:33]
	s_waitcnt vmcnt(12)
	v_mfma_f32_32x32x16_f16 v[50:65], v[2:5], v[106:109], v[50:65]
	ds_read_b128 v[2:5], v6
	ds_read_b128 v[6:9], v6 offset:32768
	v_mfma_f32_32x32x16_f16 v[18:33], v[10:13], v[118:121], v[18:33]
	s_waitcnt vmcnt(11)
	v_mfma_f32_32x32x16_f16 v[50:65], v[10:13], v[94:97], v[50:65]
	s_waitcnt vmcnt(7) lgkmcnt(1)
	v_mfma_f32_32x32x16_f16 v[34:49], v[2:5], v[66:69], 0
	v_mfma_f32_32x32x16_f16 v[18:33], v[14:17], v[114:117], v[18:33]
	v_mfma_f32_32x32x16_f16 v[50:65], v[14:17], v[90:93], v[50:65]
	v_bitop3_b32 v14, v171, s26, v170 bitop3:0x36
	ds_read_b128 v[10:13], v14
	ds_read_b128 v[14:17], v14 offset:32768
	s_nop 7
	v_cvt_pk_f16_f32 v25, v24, v25
	v_cvt_pk_f16_f32 v24, v22, v23
	v_cvt_pk_f16_f32 v23, v20, v21
	v_cvt_pk_f16_f32 v22, v18, v19
	v_cvt_pk_f16_f32 v21, v32, v33
	s_waitcnt vmcnt(6) lgkmcnt(1)
	v_mfma_f32_32x32x16_f16 v[34:49], v[10:13], v[70:73], v[34:49]
	v_cvt_pk_f16_f32 v20, v30, v31
	v_cvt_pk_f16_f32 v19, v28, v29
	v_cvt_pk_f16_f32 v18, v26, v27
	ds_write_b128 v173, v[22:25]
	ds_write_b128 v172, v[18:21]
	v_cvt_pk_f16_f32 v21, v56, v57
	v_cvt_pk_f16_f32 v20, v54, v55
	s_waitcnt vmcnt(5)
	v_mfma_f32_32x32x16_f16 v[34:49], v[6:9], v[74:77], v[34:49]
	v_cvt_pk_f16_f32 v19, v52, v53
	v_cvt_pk_f16_f32 v18, v50, v51
	ds_write_b128 v173, v[18:21] offset:32768
	v_cvt_pk_f16_f32 v21, v64, v65
	v_cvt_pk_f16_f32 v20, v62, v63
	v_cvt_pk_f16_f32 v19, v60, v61
	v_cvt_pk_f16_f32 v18, v58, v59
	s_waitcnt vmcnt(4) lgkmcnt(3)
	v_mfma_f32_32x32x16_f16 v[34:49], v[14:17], v[78:81], v[34:49]
	ds_write_b128 v172, v[18:21] offset:32768
	s_waitcnt vmcnt(3)
	v_mfma_f32_32x32x16_f16 v[66:81], v[2:5], v[82:85], 0
	s_nop 8
	v_cvt_pk_f16_f32 v41, v40, v41
	v_cvt_pk_f16_f32 v40, v38, v39
	v_cvt_pk_f16_f32 v39, v36, v37
	v_cvt_pk_f16_f32 v38, v34, v35
	v_cvt_pk_f16_f32 v85, v48, v49
	v_cvt_pk_f16_f32 v84, v46, v47
	v_cvt_pk_f16_f32 v83, v44, v45
	s_waitcnt vmcnt(2)
	v_mfma_f32_32x32x16_f16 v[66:81], v[10:13], v[86:89], v[66:81]
	v_cvt_pk_f16_f32 v82, v42, v43
	s_waitcnt vmcnt(1)
	v_mfma_f32_32x32x16_f16 v[66:81], v[6:9], v[182:185], v[66:81]
	s_waitcnt vmcnt(0)
	v_mfma_f32_32x32x16_f16 v[66:81], v[14:17], v[186:189], v[66:81]
	v_mfma_f32_32x32x16_f16 v[2:17], v[38:41], v[126:129], 0
	s_nop 10
	v_cvt_pk_f16_f32 v73, v72, v73
	v_cvt_pk_f16_f32 v72, v70, v71
	v_cvt_pk_f16_f32 v70, v66, v67
	v_cvt_pk_f16_f32 v67, v76, v77
	v_cvt_pk_f16_f32 v66, v74, v75
	global_load_dwordx4 v[74:77], v154, s[2:3]
	v_cvt_pk_f16_f32 v71, v68, v69
	v_cvt_pk_f16_f32 v69, v80, v81
	v_cvt_pk_f16_f32 v68, v78, v79
	global_load_dwordx4 v[78:81], v154, s[2:3] offset:1024
	ds_read_b128 v[18:21], v180
	ds_read_b128 v[22:25], v176
	ds_read_b128 v[26:29], v180 offset:32768
	global_load_dwordx4 v[30:33], v154, s[2:3] offset:2048
	v_mfma_f32_32x32x16_f16 v[34:49], v[38:41], v[110:113], 0
	v_mfma_f32_32x32x16_f16 v[2:17], v[82:85], v[122:125], v[2:17]
	v_mfma_f32_32x32x16_f16 v[34:49], v[82:85], v[106:109], v[34:49]
	ds_read_b128 v[82:85], v176 offset:32768
	s_waitcnt vmcnt(2) lgkmcnt(3)
	v_mfma_f32_32x32x16_f16 v[50:65], v[18:21], v[74:77], 0
	v_mfma_f32_32x32x16_f16 v[2:17], v[70:73], v[118:121], v[2:17]
	v_mfma_f32_32x32x16_f16 v[34:49], v[70:73], v[94:97], v[34:49]
	v_lshl_add_u64 v[70:71], s[2:3], 0, v[154:155]
	v_add_co_u32_e32 v152, vcc, s23, v70
	s_nop 1
	v_addc_co_u32_e32 v153, vcc, 0, v71, vcc
	s_waitcnt vmcnt(1) lgkmcnt(2)
	v_mfma_f32_32x32x16_f16 v[50:65], v[22:25], v[78:81], v[50:65]
	v_mfma_f32_32x32x16_f16 v[2:17], v[66:69], v[114:117], v[2:17]
	v_mfma_f32_32x32x16_f16 v[34:49], v[66:69], v[90:93], v[34:49]
	global_load_dwordx4 v[66:69], v154, s[2:3] offset:3072
	s_nop 9
	v_cvt_pk_f16_f32 v9, v8, v9
	v_cvt_pk_f16_f32 v8, v6, v7
	v_cvt_pk_f16_f32 v7, v4, v5
	v_cvt_pk_f16_f32 v6, v2, v3
	v_cvt_pk_f16_f32 v5, v16, v17
	v_cvt_pk_f16_f32 v4, v14, v15
	s_waitcnt vmcnt(1) lgkmcnt(1)
	v_mfma_f32_32x32x16_f16 v[50:65], v[26:29], v[30:33], v[50:65]
	global_load_dwordx4 v[30:33], v168, s[2:3]
	global_load_dwordx4 v[86:89], v[152:153], off offset:1024
	s_nop 0
	global_load_dwordx4 v[168:171], v168, s[0:1]
	v_cvt_pk_f16_f32 v3, v12, v13
	v_cvt_pk_f16_f32 v2, v10, v11
	ds_write_b128 v175, v[6:9]
	ds_write_b128 v174, v[2:5]
	v_cvt_pk_f16_f32 v5, v40, v41
	s_waitcnt vmcnt(3) lgkmcnt(2)
	v_mfma_f32_32x32x16_f16 v[50:65], v[82:85], v[66:69], v[50:65]
	global_load_dwordx4 v[182:185], v154, s[0:1] offset:1024
	v_cvt_pk_f16_f32 v4, v38, v39
	v_cvt_pk_f16_f32 v3, v36, v37
	v_cvt_pk_f16_f32 v2, v34, v35
	ds_write_b128 v175, v[2:5] offset:32768
	v_cvt_pk_f16_f32 v5, v48, v49
	v_cvt_pk_f16_f32 v4, v46, v47
	s_waitcnt vmcnt(3)
	v_mfma_f32_32x32x16_f16 v[66:81], v[18:21], v[30:33], 0
	global_load_dwordx4 v[18:21], v[152:153], off offset:2048
	v_cvt_pk_f16_f32 v3, v44, v45
	v_cvt_pk_f16_f32 v2, v42, v43
	ds_write_b128 v174, v[2:5] offset:32768
	v_cvt_pk_f16_f32 v57, v56, v57
	v_cvt_pk_f16_f32 v56, v54, v55
	v_cvt_pk_f16_f32 v55, v52, v53
	s_waitcnt vmcnt(3)
	v_mfma_f32_32x32x16_f16 v[66:81], v[22:25], v[86:89], v[66:81]
	global_load_dwordx4 v[22:25], v[152:153], off offset:3072
	v_cvt_pk_f16_f32 v54, v50, v51
	s_waitcnt vmcnt(1)
	v_mfma_f32_32x32x16_f16 v[66:81], v[26:29], v[18:21], v[66:81]
	v_lshl_add_u64 v[18:19], s[0:1], 0, v[154:155]
	v_add_co_u32_e32 v152, vcc, s23, v18
	s_nop 1
	v_addc_co_u32_e32 v153, vcc, 0, v19, vcc
	global_load_dwordx4 v[86:89], v[152:153], off offset:1024
	s_waitcnt vmcnt(1)
	v_mfma_f32_32x32x16_f16 v[66:81], v[82:85], v[22:25], v[66:81]
	v_cvt_pk_f16_f32 v85, v64, v65
	v_cvt_pk_f16_f32 v84, v62, v63
	v_cvt_pk_f16_f32 v83, v60, v61
	v_cvt_pk_f16_f32 v82, v58, v59
	v_mfma_f32_32x32x16_f16 v[18:33], v[54:57], v[126:129], 0
	s_nop 6
	v_cvt_pk_f16_f32 v73, v72, v73
	v_cvt_pk_f16_f32 v72, v70, v71
	v_cvt_pk_f16_f32 v70, v66, v67
	v_cvt_pk_f16_f32 v67, v76, v77
	v_cvt_pk_f16_f32 v66, v74, v75
	global_load_dwordx4 v[74:77], v154, s[0:1]
	ds_read_b128 v[2:5], v181
	ds_read_b128 v[6:9], v177
	ds_read_b128 v[10:13], v181 offset:32768
	global_load_dwordx4 v[14:17], v154, s[0:1] offset:2048
	global_load_dwordx4 v[34:37], v154, s[0:1] offset:3072
	v_mfma_f32_32x32x16_f16 v[50:65], v[54:57], v[110:113], 0
	v_cvt_pk_f16_f32 v71, v68, v69
	v_cvt_pk_f16_f32 v69, v80, v81
	v_cvt_pk_f16_f32 v68, v78, v79
	v_mfma_f32_32x32x16_f16 v[18:33], v[82:85], v[122:125], v[18:33]
	v_mfma_f32_32x32x16_f16 v[50:65], v[82:85], v[106:109], v[50:65]
	ds_read_b128 v[82:85], v177 offset:32768
	v_mfma_f32_32x32x16_f16 v[18:33], v[70:73], v[118:121], v[18:33]
	v_mfma_f32_32x32x16_f16 v[50:65], v[70:73], v[94:97], v[50:65]
	v_mfma_f32_32x32x16_f16 v[18:33], v[66:69], v[114:117], v[18:33]
	v_mfma_f32_32x32x16_f16 v[50:65], v[66:69], v[90:93], v[50:65]
	s_nop 10
	v_cvt_pk_f16_f32 v25, v24, v25
	v_cvt_pk_f16_f32 v24, v22, v23
	v_cvt_pk_f16_f32 v23, v20, v21
	v_cvt_pk_f16_f32 v22, v18, v19
	ds_write_b128 v132, v[22:25]
	s_waitcnt vmcnt(2) lgkmcnt(4)
	v_mfma_f32_32x32x16_f16 v[66:81], v[2:5], v[74:77], 0
	s_waitcnt lgkmcnt(3)
	v_mfma_f32_32x32x16_f16 v[66:81], v[6:9], v[182:185], v[66:81]
	s_waitcnt vmcnt(1) lgkmcnt(2)
	v_mfma_f32_32x32x16_f16 v[66:81], v[10:13], v[14:17], v[66:81]
	s_waitcnt vmcnt(0) lgkmcnt(1)
	v_mfma_f32_32x32x16_f16 v[66:81], v[82:85], v[34:37], v[66:81]
	v_mfma_f32_32x32x16_f16 v[34:49], v[2:5], v[168:171], 0
	global_load_dwordx4 v[2:5], v[152:153], off offset:2048
	s_nop 9
	v_cvt_pk_f16_f32 v73, v72, v73
	v_cvt_pk_f16_f32 v72, v70, v71
	v_cvt_pk_f16_f32 v71, v68, v69
	v_cvt_pk_f16_f32 v70, v66, v67
	v_cvt_pk_f16_f32 v69, v80, v81
	v_cvt_pk_f16_f32 v68, v78, v79
	v_mfma_f32_32x32x16_f16 v[34:49], v[6:9], v[86:89], v[34:49]
	global_load_dwordx4 v[6:9], v[152:153], off offset:3072
	v_cvt_pk_f16_f32 v67, v76, v77
	v_cvt_pk_f16_f32 v66, v74, v75
	s_waitcnt vmcnt(1)
	v_mfma_f32_32x32x16_f16 v[34:49], v[10:13], v[2:5], v[34:49]
	s_waitcnt vmcnt(0)
	v_mfma_f32_32x32x16_f16 v[34:49], v[82:85], v[6:9], v[34:49]
	v_mfma_f32_32x32x16_f16 v[2:17], v[70:73], v[126:129], 0
	s_nop 10
	v_cvt_pk_f16_f32 v41, v40, v41
	v_cvt_pk_f16_f32 v40, v38, v39
	v_cvt_pk_f16_f32 v38, v34, v35
	v_cvt_pk_f16_f32 v35, v44, v45
	v_cvt_pk_f16_f32 v34, v42, v43
	v_cvt_pk_f16_f32 v45, v32, v33
	v_cvt_pk_f16_f32 v44, v30, v31
	v_cvt_pk_f16_f32 v43, v28, v29
	v_cvt_pk_f16_f32 v42, v26, v27
	v_mfma_f32_32x32x16_f16 v[18:33], v[70:73], v[110:113], 0
	v_cvt_pk_f16_f32 v39, v36, v37
	v_cvt_pk_f16_f32 v37, v48, v49
	v_cvt_pk_f16_f32 v36, v46, v47
	ds_write_b128 v131, v[42:45]
	v_cvt_pk_f16_f32 v45, v56, v57
	v_cvt_pk_f16_f32 v44, v54, v55
	v_cvt_pk_f16_f32 v43, v52, v53
	v_mfma_f32_32x32x16_f16 v[2:17], v[66:69], v[122:125], v[2:17]
	v_cvt_pk_f16_f32 v42, v50, v51
	ds_write_b128 v132, v[42:45] offset:32768
	v_cvt_pk_f16_f32 v45, v64, v65
	v_cvt_pk_f16_f32 v44, v62, v63
	v_cvt_pk_f16_f32 v43, v60, v61
	v_cvt_pk_f16_f32 v42, v58, v59
	ds_write_b128 v131, v[42:45] offset:32768
	v_mfma_f32_32x32x16_f16 v[18:33], v[66:69], v[106:109], v[18:33]
	v_mfma_f32_32x32x16_f16 v[2:17], v[38:41], v[118:121], v[2:17]
	v_mfma_f32_32x32x16_f16 v[18:33], v[38:41], v[94:97], v[18:33]
	v_mfma_f32_32x32x16_f16 v[2:17], v[34:37], v[114:117], v[2:17]
	v_mfma_f32_32x32x16_f16 v[18:33], v[34:37], v[90:93], v[18:33]
	s_nop 10
	v_cvt_pk_f16_f32 v9, v8, v9
	v_cvt_pk_f16_f32 v8, v6, v7
	v_cvt_pk_f16_f32 v7, v4, v5
	v_cvt_pk_f16_f32 v6, v2, v3
	v_cvt_pk_f16_f32 v5, v16, v17
	v_cvt_pk_f16_f32 v4, v14, v15
	v_cvt_pk_f16_f32 v3, v12, v13
	v_cvt_pk_f16_f32 v2, v10, v11
	ds_write_b128 v135, v[6:9]
	ds_write_b128 v133, v[2:5]
	v_cvt_pk_f16_f32 v5, v24, v25
	v_cvt_pk_f16_f32 v4, v22, v23
	v_cvt_pk_f16_f32 v3, v20, v21
	v_cvt_pk_f16_f32 v2, v18, v19
	ds_write_b128 v135, v[2:5] offset:32768
	v_cvt_pk_f16_f32 v5, v32, v33
	v_cvt_pk_f16_f32 v4, v30, v31
	v_cvt_pk_f16_f32 v3, v28, v29
	v_cvt_pk_f16_f32 v2, v26, v27
	ds_write_b128 v133, v[2:5] offset:32768
	s_setprio 0
	s_waitcnt lgkmcnt(0)
	s_barrier
	ds_read_b64_tr_b16 v[2:3], v146
	ds_read_b64_tr_b16 v[4:5], v147
	ds_read_b64_tr_b16 v[36:37], v147 offset:32768
	ds_read_b64_tr_b16 v[34:35], v146 offset:32768
	ds_read_b64_tr_b16 v[18:19], v150
	ds_read_b64_tr_b16 v[20:21], v151
	ds_read_b64_tr_b16 v[40:41], v151 offset:32768
	ds_read_b64_tr_b16 v[38:39], v150 offset:32768
	s_waitcnt lgkmcnt(6)
	v_mfma_f32_32x32x16_f16 v[2:17], v[2:5], v[102:105], 0
	ds_read_b64_tr_b16 v[42:43], v148
	ds_read_b64_tr_b16 v[44:45], v149
	ds_read_b64_tr_b16 v[48:49], v149 offset:32768
	ds_read_b64_tr_b16 v[46:47], v148 offset:32768
	v_cmp_gt_u32_e64 s[0:1], 32, v167
	s_cmp_eq_u32 s5, 0
	v_cmp_lt_i32_e64 s[2:3], v162, v163
	s_waitcnt lgkmcnt(6)
	v_mfma_f32_32x32x16_f16 v[18:33], v[18:21], v[102:105], 0
	v_mfma_f32_32x32x16_f16 v[2:17], v[34:37], v[98:101], v[2:17]
	s_waitcnt lgkmcnt(4)
	v_mfma_f32_32x32x16_f16 v[18:33], v[38:41], v[98:101], v[18:33]
	s_nop 9
	v_mul_f32_e64 v34, v16, v16
	v_mul_f32_e64 v35, v17, v17
	v_mul_f32_e64 v36, v12, v12
	v_mul_f32_e64 v37, v13, v13
	v_mul_f32_e64 v50, v8, v8
	v_mul_f32_e64 v51, v9, v9
	v_pk_mul_f32 v[52:53], v[4:5], v[4:5]
	v_pk_fma_f32 v[50:51], v[6:7], v[6:7], v[50:51]
	v_pk_fma_f32 v[52:53], v[2:3], v[2:3], v[52:53]
	v_pk_fma_f32 v[36:37], v[10:11], v[10:11], v[36:37]
	v_pk_fma_f32 v[34:35], v[14:15], v[14:15], v[34:35]
	v_pk_mul_f32 v[116:117], v[24:25], v[24:25]
	v_pk_mul_f32 v[118:119], v[20:21], v[20:21]
	v_pk_add_f32 v[50:51], v[52:53], v[50:51]
	v_pk_add_f32 v[34:35], v[36:37], v[34:35]
	v_pk_mul_f32 v[112:113], v[32:33], v[32:33]
	v_pk_mul_f32 v[114:115], v[28:29], v[28:29]
	v_pk_mul_f32 v[120:121], v[18:19], v[18:19]
	v_pk_fma_f32 v[18:19], v[18:19], v[18:19], v[118:119]
	v_pk_fma_f32 v[20:21], v[22:23], v[22:23], v[116:117]
	v_pk_add_f32 v[34:35], v[50:51], v[34:35]
	v_pk_mul_f32 v[106:107], v[22:23], v[22:23]
	v_pk_add_f32 v[18:19], v[18:19], v[20:21]
	v_pk_fma_f32 v[20:21], v[26:27], v[26:27], v[114:115]
	v_pk_fma_f32 v[22:23], v[30:31], v[30:31], v[112:113]
	v_add_f32_e32 v34, v34, v35
	v_pk_add_f32 v[20:21], v[20:21], v[22:23]
	v_add_f32_e32 v36, 0, v34
	v_pk_mul_f32 v[108:109], v[26:27], v[26:27]
	v_pk_mul_f32 v[110:111], v[30:31], v[30:31]
	v_pk_add_f32 v[34:35], v[18:19], v[20:21]
	s_waitcnt lgkmcnt(2)
	v_mfma_f32_32x32x16_f16 v[18:33], v[42:45], v[102:105], 0
	v_add_f32_e32 v34, v34, v35
	v_add_f32_e32 v54, v36, v34
	v_sub_f32_e32 v55, v36, v34
	ds_read_b64_tr_b16 v[34:35], v144
	ds_read_b64_tr_b16 v[36:37], v145
	ds_read_b64_tr_b16 v[52:53], v145 offset:32768
	ds_read_b64_tr_b16 v[50:51], v144 offset:32768
	v_pk_fma_f32 v[4:5], v[4:5], v[4:5], v[118:119]
	v_pk_fma_f32 v[16:17], v[16:17], v[16:17], v[112:113]
	v_pk_fma_f32 v[14:15], v[14:15], v[14:15], v[110:111]
	s_waitcnt lgkmcnt(4)
	v_mfma_f32_32x32x16_f16 v[18:33], v[46:49], v[98:101], v[18:33]
	v_fma_f32 v12, v12, v12, v114
	v_fma_f32 v13, v13, v13, v115
	v_fma_f32 v10, v10, v10, v108
	v_fma_f32 v11, v11, v11, v109
	v_fma_f32 v8, v8, v8, v116
	v_fma_f32 v9, v9, v9, v117
	v_pk_fma_f32 v[6:7], v[6:7], v[6:7], v[106:107]
	v_pk_fma_f32 v[2:3], v[2:3], v[2:3], v[120:121]
	s_nop 3
	v_pk_mul_f32 v[38:39], v[32:33], v[32:33]
	v_pk_mul_f32 v[40:41], v[28:29], v[28:29]
	v_pk_mul_f32 v[42:43], v[24:25], v[24:25]
	v_pk_mul_f32 v[44:45], v[20:21], v[20:21]
	v_pk_fma_f32 v[42:43], v[22:23], v[22:23], v[42:43]
	v_pk_fma_f32 v[44:45], v[18:19], v[18:19], v[44:45]
	v_pk_fma_f32 v[40:41], v[26:27], v[26:27], v[40:41]
	v_pk_fma_f32 v[38:39], v[30:31], v[30:31], v[38:39]
	v_pk_add_f32 v[42:43], v[44:45], v[42:43]
	v_pk_add_f32 v[38:39], v[40:41], v[38:39]
	v_pk_fma_f32 v[4:5], v[20:21], v[20:21], v[4:5]
	v_pk_add_f32 v[38:39], v[42:43], v[38:39]
	v_pk_fma_f32 v[6:7], v[22:23], v[22:23], v[6:7]
	v_add_f32_e32 v56, v38, v39
	s_waitcnt lgkmcnt(2)
	v_mfma_f32_32x32x16_f16 v[34:49], v[34:37], v[102:105], 0
	v_add_f32_e32 v70, v54, v56
	v_add_f32_e32 v71, v55, v56
	v_sub_f32_e32 v72, v54, v56
	ds_read_b64_tr_b16 v[54:55], v142
	ds_read_b64_tr_b16 v[56:57], v143
	ds_read_b64_tr_b16 v[68:69], v143 offset:32768
	ds_read_b64_tr_b16 v[66:67], v142 offset:32768
	v_pk_fma_f32 v[8:9], v[24:25], v[24:25], v[8:9]
	v_pk_fma_f32 v[10:11], v[26:27], v[26:27], v[10:11]
	v_pk_fma_f32 v[12:13], v[28:29], v[28:29], v[12:13]
	s_waitcnt lgkmcnt(4)
	v_mfma_f32_32x32x16_f16 v[34:49], v[50:53], v[98:101], v[34:49]
	v_fma_f32 v14, v30, v30, v14
	v_fma_f32 v15, v31, v31, v15
	v_fma_f32 v16, v32, v32, v16
	v_fma_f32 v17, v33, v33, v17
	v_fma_f32 v2, v18, v18, v2
	v_fma_f32 v3, v19, v19, v3
	s_nop 5
	v_pk_mul_f32 v[50:51], v[48:49], v[48:49]
	v_pk_mul_f32 v[52:53], v[44:45], v[44:45]
	v_pk_mul_f32 v[58:59], v[40:41], v[40:41]
	v_pk_mul_f32 v[60:61], v[36:37], v[36:37]
	v_pk_fma_f32 v[58:59], v[38:39], v[38:39], v[58:59]
	v_pk_fma_f32 v[60:61], v[34:35], v[34:35], v[60:61]
	v_pk_fma_f32 v[52:53], v[42:43], v[42:43], v[52:53]
	v_pk_fma_f32 v[50:51], v[46:47], v[46:47], v[50:51]
	v_pk_add_f32 v[58:59], v[60:61], v[58:59]
	v_pk_add_f32 v[50:51], v[52:53], v[50:51]
	v_pk_fma_f32 v[4:5], v[36:37], v[36:37], v[4:5]
	v_pk_add_f32 v[50:51], v[58:59], v[50:51]
	v_pk_fma_f32 v[16:17], v[48:49], v[48:49], v[16:17]
	v_add_f32_e32 v73, v50, v51
	s_waitcnt lgkmcnt(2)
	v_mfma_f32_32x32x16_f16 v[50:65], v[54:57], v[102:105], 0
	v_add_f32_e32 v86, v70, v73
	v_sub_f32_e32 v87, v71, v73
	v_sub_f32_e32 v88, v72, v73
	ds_read_b64_tr_b16 v[70:71], v140
	ds_read_b64_tr_b16 v[72:73], v141
	ds_read_b64_tr_b16 v[84:85], v141 offset:32768
	ds_read_b64_tr_b16 v[82:83], v140 offset:32768
	v_pk_fma_f32 v[14:15], v[46:47], v[46:47], v[14:15]
	v_pk_fma_f32 v[12:13], v[44:45], v[44:45], v[12:13]
	v_pk_fma_f32 v[10:11], v[42:43], v[42:43], v[10:11]
	s_waitcnt lgkmcnt(4)
	v_mfma_f32_32x32x16_f16 v[50:65], v[66:69], v[98:101], v[50:65]
	v_fma_f32 v8, v40, v40, v8
	v_fma_f32 v9, v41, v41, v9
	v_fma_f32 v6, v38, v38, v6
	v_fma_f32 v7, v39, v39, v7
	v_fma_f32 v2, v34, v34, v2
	v_fma_f32 v3, v35, v35, v3
	s_nop 5
	v_pk_mul_f32 v[66:67], v[64:65], v[64:65]
	v_pk_mul_f32 v[68:69], v[60:61], v[60:61]
	v_pk_mul_f32 v[74:75], v[56:57], v[56:57]
	v_pk_mul_f32 v[76:77], v[52:53], v[52:53]
	v_pk_fma_f32 v[74:75], v[54:55], v[54:55], v[74:75]
	v_pk_fma_f32 v[76:77], v[50:51], v[50:51], v[76:77]
	v_pk_fma_f32 v[68:69], v[58:59], v[58:59], v[68:69]
	v_pk_fma_f32 v[66:67], v[62:63], v[62:63], v[66:67]
	v_pk_add_f32 v[74:75], v[76:77], v[74:75]
	v_pk_add_f32 v[66:67], v[68:69], v[66:67]
	v_pk_fma_f32 v[4:5], v[52:53], v[52:53], v[4:5]
	v_pk_add_f32 v[66:67], v[74:75], v[66:67]
	v_pk_fma_f32 v[6:7], v[54:55], v[54:55], v[6:7]
	v_add_f32_e32 v89, v66, v67
	s_waitcnt lgkmcnt(2)
	v_mfma_f32_32x32x16_f16 v[66:81], v[70:73], v[102:105], 0
	v_add_f32_e32 v94, v86, v89
	v_add_f32_e32 v126, v87, v89
	v_add_f32_e32 v127, v88, v89
	v_sub_f32_e32 v128, v86, v89
	ds_read_b64_tr_b16 v[86:87], v138
	ds_read_b64_tr_b16 v[88:89], v139
	ds_read_b64_tr_b16 v[124:125], v139 offset:32768
	ds_read_b64_tr_b16 v[122:123], v138 offset:32768
	v_pk_fma_f32 v[8:9], v[56:57], v[56:57], v[8:9]
	v_pk_fma_f32 v[10:11], v[58:59], v[58:59], v[10:11]
	s_waitcnt lgkmcnt(4)
	v_mfma_f32_32x32x16_f16 v[66:81], v[82:85], v[98:101], v[66:81]
	v_fma_f32 v12, v60, v60, v12
	v_fma_f32 v13, v61, v61, v13
	v_fma_f32 v14, v62, v62, v14
	v_fma_f32 v15, v63, v63, v15
	v_fma_f32 v16, v64, v64, v16
	v_fma_f32 v17, v65, v65, v17
	v_pk_fma_f32 v[2:3], v[50:51], v[50:51], v[2:3]
	s_nop 4
	v_pk_mul_f32 v[82:83], v[80:81], v[80:81]
	v_pk_mul_f32 v[84:85], v[76:77], v[76:77]
	v_pk_mul_f32 v[90:91], v[72:73], v[72:73]
	v_pk_mul_f32 v[92:93], v[68:69], v[68:69]
	v_pk_fma_f32 v[90:91], v[70:71], v[70:71], v[90:91]
	v_pk_fma_f32 v[92:93], v[66:67], v[66:67], v[92:93]
	v_pk_fma_f32 v[84:85], v[74:75], v[74:75], v[84:85]
	v_pk_fma_f32 v[82:83], v[78:79], v[78:79], v[82:83]
	v_pk_add_f32 v[90:91], v[92:93], v[90:91]
	v_pk_add_f32 v[82:83], v[84:85], v[82:83]
	v_pk_fma_f32 v[4:5], v[68:69], v[68:69], v[4:5]
	v_pk_add_f32 v[82:83], v[90:91], v[82:83]
	v_pk_fma_f32 v[18:19], v[80:81], v[80:81], v[16:17]
	v_add_f32_e32 v129, v82, v83
	v_add_f32_e32 v131, v94, v129
	s_waitcnt lgkmcnt(2)
	v_mfma_f32_32x32x16_f16 v[82:97], v[86:89], v[102:105], 0
	v_sub_f32_e32 v135, v126, v129
	v_add_f32_e32 v142, v127, v129
	v_sub_f32_e32 v143, v128, v129
	ds_read_b64_tr_b16 v[126:127], v136
	ds_read_b64_tr_b16 v[128:129], v137
	ds_read_b64_tr_b16 v[138:139], v137 offset:32768
	ds_read_b64_tr_b16 v[136:137], v136 offset:32768
	v_pk_fma_f32 v[20:21], v[78:79], v[78:79], v[14:15]
	v_pk_fma_f32 v[22:23], v[76:77], v[76:77], v[12:13]
	v_pk_fma_f32 v[24:25], v[74:75], v[74:75], v[10:11]
	s_waitcnt lgkmcnt(4)
	v_mfma_f32_32x32x16_f16 v[82:97], v[122:125], v[98:101], v[82:97]
	v_fma_f32 v26, v72, v72, v8
	v_fma_f32 v27, v73, v73, v9
	v_fma_f32 v28, v70, v70, v6
	v_fma_f32 v29, v71, v71, v7
	v_fma_f32 v30, v66, v66, v2
	v_fma_f32 v31, v67, v67, v3
	s_nop 5
	v_pk_fma_f32 v[32:33], v[84:85], v[84:85], v[4:5]
	s_waitcnt lgkmcnt(2)
	v_mfma_f32_32x32x16_f16 v[2:17], v[126:129], v[102:105], 0
	v_fma_f32 v28, v86, v86, v28
	v_fma_f32 v29, v87, v87, v29
	v_fma_f32 v24, v90, v90, v24
	v_fma_f32 v25, v91, v91, v25
	v_fma_f32 v22, v92, v92, v22
	v_fma_f32 v23, v93, v93, v23
	v_pk_fma_f32 v[20:21], v[94:95], v[94:95], v[20:21]
	v_pk_fma_f32 v[18:19], v[96:97], v[96:97], v[18:19]
	v_pk_fma_f32 v[30:31], v[82:83], v[82:83], v[30:31]
	v_pk_fma_f32 v[26:27], v[88:89], v[88:89], v[26:27]
	s_waitcnt lgkmcnt(0)
	v_mfma_f32_32x32x16_f16 v[2:17], v[136:139], v[98:101], v[2:17]
	v_mul_f32_e64 v122, v96, v96
	v_mul_f32_e64 v123, v97, v97
	v_mul_f32_e64 v124, v92, v92
	v_mul_f32_e64 v125, v93, v93
	v_mul_f32_e64 v132, v88, v88
	v_mul_f32_e64 v133, v89, v89
	v_pk_mul_f32 v[140:141], v[84:85], v[84:85]
	v_pk_fma_f32 v[132:133], v[86:87], v[86:87], v[132:133]
	v_pk_fma_f32 v[140:141], v[82:83], v[82:83], v[140:141]
	v_pk_fma_f32 v[124:125], v[90:91], v[90:91], v[124:125]
	s_nop 1
	v_pk_mul_f32 v[38:39], v[8:9], v[8:9]
	v_pk_mul_f32 v[40:41], v[4:5], v[4:5]
	v_pk_mul_f32 v[34:35], v[16:17], v[16:17]
	v_pk_mul_f32 v[36:37], v[12:13], v[12:13]
	v_pk_fma_f32 v[16:17], v[16:17], v[16:17], v[18:19]
	v_pk_fma_f32 v[18:19], v[14:15], v[14:15], v[20:21]
	v_pk_fma_f32 v[12:13], v[12:13], v[12:13], v[22:23]
	v_pk_fma_f32 v[20:21], v[10:11], v[10:11], v[24:25]
	v_pk_fma_f32 v[22:23], v[6:7], v[6:7], v[28:29]
	v_pk_fma_f32 v[24:25], v[2:3], v[2:3], v[30:31]
	v_pk_fma_f32 v[2:3], v[2:3], v[2:3], v[40:41]
	v_pk_fma_f32 v[6:7], v[6:7], v[6:7], v[38:39]
	v_pk_fma_f32 v[4:5], v[4:5], v[4:5], v[32:33]
	v_pk_add_f32 v[2:3], v[2:3], v[6:7]
	v_pk_fma_f32 v[6:7], v[10:11], v[10:11], v[36:37]
	v_pk_fma_f32 v[10:11], v[14:15], v[14:15], v[34:35]
	v_pk_fma_f32 v[8:9], v[8:9], v[8:9], v[26:27]
	v_pk_add_f32 v[6:7], v[6:7], v[10:11]
	v_sub_f32_e32 v10, v24, v25
	v_add_f32_e32 v11, v25, v24
	v_add_f32_e32 v10, v4, v10
	v_sub_f32_e32 v14, v11, v4
	v_add_f32_e32 v4, v4, v11
	v_sub_f32_e32 v10, v10, v5
	v_sub_f32_e32 v11, v14, v5
	v_add_f32_e32 v4, v5, v4
	v_add_f32_e32 v5, v22, v10
	v_add_f32_e32 v10, v22, v11
	v_sub_f32_e32 v11, v4, v22
	v_add_f32_e32 v4, v22, v4
	v_sub_f32_e32 v5, v5, v23
	v_add_f32_e32 v10, v23, v10
	v_sub_f32_e32 v11, v11, v23
	v_add_f32_e32 v4, v23, v4
	v_add_f32_e32 v5, v8, v5
	v_sub_f32_e32 v10, v10, v8
	v_sub_f32_e32 v11, v11, v8
	v_add_f32_e32 v4, v8, v4
	v_sub_f32_e32 v5, v5, v9
	v_pk_fma_f32 v[122:123], v[94:95], v[94:95], v[122:123]
	v_sub_f32_e32 v8, v10, v9
	v_sub_f32_e32 v10, v11, v9
	v_add_f32_e32 v4, v9, v4
	v_add_f32_e32 v5, v20, v5
	v_pk_add_f32 v[132:133], v[140:141], v[132:133]
	v_pk_add_f32 v[122:123], v[124:125], v[122:123]
	v_add_f32_e32 v8, v20, v8
	v_add_f32_e32 v9, v20, v10
	v_sub_f32_e32 v4, v4, v20
	v_sub_f32_e32 v5, v5, v21
	v_pk_add_f32 v[122:123], v[132:133], v[122:123]
	v_add_f32_e32 v8, v21, v8
	v_add_f32_e32 v9, v21, v9
	v_sub_f32_e32 v4, v4, v21
	v_add_f32_e32 v5, v12, v5
	v_add_f32_e32 v122, v122, v123
	v_pk_add_f32 v[2:3], v[2:3], v[6:7]
	v_sub_f32_e32 v8, v8, v12
	v_add_f32_e32 v9, v12, v9
	v_sub_f32_e32 v4, v4, v12
	v_sub_f32_e32 v5, v5, v13
	v_add_f32_e32 v123, v131, v122
	v_add_f32_e32 v2, v2, v3
	v_sub_f32_e32 v8, v8, v13
	v_add_f32_e32 v9, v13, v9
	v_sub_f32_e32 v4, v4, v13
	v_add_f32_e32 v5, v18, v5
	v_add_f32_e32 v3, v123, v2
	v_add_f32_e32 v8, v18, v8
	v_sub_f32_e32 v9, v9, v18
	v_sub_f32_e32 v4, v4, v18
	v_sub_f32_e32 v5, v5, v19
	v_and_b32_e32 v10, 8, v156
	v_add_f32_e32 v8, v19, v8
	v_sub_f32_e32 v9, v9, v19
	v_sub_f32_e32 v4, v4, v19
	v_add_f32_e32 v5, v16, v5
	v_cmp_eq_u32_e32 vcc, 0, v10
	v_cndmask_b32_e64 v10, -v3, v3, s[0:1]
	s_cselect_b64 s[0:1], -1, 0
	s_bitcmp0_b32 s4, 7
	v_sub_f32_e32 v8, v8, v16
	v_sub_f32_e32 v9, v9, v16
	v_sub_f32_e32 v4, v4, v16
	v_sub_f32_e32 v5, v5, v17
	v_cndmask_b32_e64 v11, -v3, v3, s[0:1]
	s_cselect_b64 s[0:1], -1, 0
	v_and_b32_e32 v16, 32, v156
	v_sub_f32_e32 v8, v8, v17
	v_cndmask_b32_e64 v5, -v5, v5, vcc
	v_cndmask_b32_e64 v12, -v3, v3, s[0:1]
	v_cndmask_b32_e64 v18, v161, v162, s[2:3]
	v_cmp_eq_u32_e64 s[2:3], 0, v16
	v_lshlrev_b32_e32 v18, 2, v18
	v_cmp_eq_u32_e64 s[0:1], 0, v134
	v_cndmask_b32_e64 v16, v11, v5, s[2:3]
	v_cndmask_b32_e64 v5, v5, v11, s[2:3]
	v_cndmask_b32_e64 v11, v8, v12, s[2:3]
	ds_bpermute_b32 v11, v18, v11
	v_and_b32_e32 v14, 2, v156
	v_cndmask_b32_e64 v13, -v3, v3, s[0:1]
	v_cmp_eq_u32_e64 s[0:1], 0, v14
	v_cndmask_b32_e64 v8, v12, v8, s[2:3]
	v_add_f32_e32 v124, v135, v122
	v_cndmask_b32_e64 v14, -v3, v3, s[0:1]
	v_cmp_eq_u32_e64 s[0:1], 0, v130
	v_sub_f32_e32 v4, v4, v17
	s_waitcnt lgkmcnt(0)
	v_add_f32_e32 v8, v8, v11
	v_cndmask_b32_e64 v15, -v3, v3, s[0:1]
	v_cndmask_b32_e64 v11, v14, v10, s[2:3]
	v_cndmask_b32_e64 v10, v10, v14, s[2:3]
	v_sub_f32_e32 v6, v124, v2
	v_sub_f32_e32 v9, v9, v17
	v_cndmask_b32_e64 v3, -v3, v3, vcc
	ds_bpermute_b32 v10, v18, v10
	v_cndmask_b32_e64 v12, v4, v15, s[2:3]
	v_sub_f32_e32 v125, v142, v122
	v_cndmask_b32_e64 v19, v9, v13, s[2:3]
	v_cndmask_b32_e64 v9, v13, v9, s[2:3]
	ds_bpermute_b32 v12, v18, v12
	v_cndmask_b32_e64 v13, v6, v3, s[2:3]
	v_sub_f32_e32 v7, v125, v2
	v_bfe_i32 v17, v156, 5, 1
	ds_bpermute_b32 v5, v18, v5
	ds_bpermute_b32 v13, v18, v13
	v_sub_f32_e32 v122, v143, v122
	v_cndmask_b32_e64 v3, v3, v6, s[2:3]
	v_and_b32_e32 v6, v17, v7
	v_sub_f32_e32 v2, v122, v2
	ds_bpermute_b32 v19, v18, v19
	ds_bpermute_b32 v6, v18, v6
	s_waitcnt lgkmcnt(5)
	v_add_f32_e32 v10, v11, v10
	v_cndmask_b32_e64 v4, v15, v4, s[2:3]
	v_and_b32_e32 v11, v17, v2
	s_waitcnt lgkmcnt(4)
	v_add_f32_e32 v4, v4, v12
	ds_bpermute_b32 v11, v18, v11
	v_and_b32_e32 v12, 16, v156
	v_cmp_lt_i32_e64 s[4:5], v164, v163
	s_waitcnt lgkmcnt(4)
	v_add_f32_e32 v5, v16, v5
	s_waitcnt lgkmcnt(3)
	v_add_f32_e32 v3, v3, v13
	v_cndmask_b32_e64 v13, v161, v164, s[4:5]
	v_cmp_eq_u32_e64 s[4:5], 0, v12
	s_waitcnt lgkmcnt(2)
	v_add_f32_e32 v9, v9, v19
	v_lshlrev_b32_e32 v13, 2, v13
	v_cndmask_b32_e64 v12, v4, v5, s[4:5]
	v_cndmask_b32_e64 v4, v5, v4, s[4:5]
	v_cndmask_b32_e64 v5, 0, v7, s[2:3]
	s_waitcnt lgkmcnt(1)
	v_add_f32_e32 v5, v5, v6
	v_cndmask_b32_e64 v2, 0, v2, s[2:3]
	v_cndmask_b32_e64 v7, v9, v5, s[4:5]
	ds_bpermute_b32 v4, v13, v4
	s_waitcnt lgkmcnt(1)
	v_add_f32_e32 v2, v2, v11
	v_cndmask_b32_e64 v6, v3, v8, s[4:5]
	v_cndmask_b32_e64 v3, v8, v3, s[4:5]
	ds_bpermute_b32 v7, v13, v7
	ds_bpermute_b32 v3, v13, v3
	v_cndmask_b32_e64 v8, v10, v2, s[4:5]
	ds_bpermute_b32 v8, v13, v8
	v_cndmask_b32_e64 v5, v5, v9, s[4:5]
	s_waitcnt lgkmcnt(3)
	v_add_f32_e32 v4, v12, v4
	s_waitcnt lgkmcnt(2)
	v_add_f32_e32 v5, v5, v7
	s_waitcnt lgkmcnt(1)
	v_add_f32_e32 v3, v6, v3
	v_cndmask_b32_e64 v2, v2, v10, s[4:5]
	v_cndmask_b32_e32 v6, v5, v4, vcc
	v_cndmask_b32_e32 v4, v4, v5, vcc
	v_mov_b32_e32 v5, v155
	s_waitcnt lgkmcnt(0)
	v_add_f32_e32 v2, v2, v8
	v_mov_b32_dpp v5, v4 row_mirror row_mask:0xf bank_mask:0xf
	s_nop 1
	v_add_f32_dpp v4, v5, v6 row_half_mirror row_mask:0xf bank_mask:0xf bound_ctrl:1
	v_cndmask_b32_e32 v5, v2, v3, vcc
	v_cndmask_b32_e32 v2, v3, v2, vcc
	v_mov_b32_e32 v3, v155
	s_nop 1
	v_mov_b32_dpp v3, v2 row_mirror row_mask:0xf bank_mask:0xf
	s_nop 1
	v_add_f32_dpp v2, v3, v5 row_half_mirror row_mask:0xf bank_mask:0xf bound_ctrl:1
	v_cndmask_b32_e64 v3, v2, v4, s[0:1]
	v_cndmask_b32_e64 v2, v4, v2, s[0:1]
	v_mov_b32_e32 v4, v155
	s_nop 1
	v_mov_b32_dpp v4, v2 row_half_mirror row_mask:0xf bank_mask:0xf
	s_nop 1
	v_add_f32_dpp v2, v4, v3 quad_perm:[3,2,1,0] row_mask:0xf bank_mask:0xf bound_ctrl:1
	v_and_b32_e32 v4, 3, v156
	v_cmp_eq_u32_e32 vcc, 0, v4
	v_and_b32_e32 v4, 56, v156
	v_add_f32_dpp v2, v2, v2 quad_perm:[2,3,0,1] row_mask:0xf bank_mask:0xf bound_ctrl:1
	v_mov_b32_e32 v3, 0
	v_cmp_ne_u32_e64 s[0:1], 56, v4
	s_and_b64 s[2:3], vcc, s[0:1]
	v_mov_b32_dpp v3, v2 quad_perm:[1,0,3,2] row_mask:0xf bank_mask:0xf
	s_and_saveexec_b64 s[0:1], s[2:3]
	v_and_b32_e32 v4, 0xfc, v156
	v_add_f32_e32 v2, v2, v3
	v_or_b32_e32 v4, v165, v4
	ds_write_b32 v4, v2
	s_or_b64 exec, exec, s[0:1]
	v_cmp_gt_i32_e32 vcc, 14, v156
	s_waitcnt lgkmcnt(0)
	s_barrier
	s_and_saveexec_b64 s[0:1], vcc
	s_cbranch_execz .LBB1_2
	ds_read_b32 v2, v166
	ds_read_b32 v3, v166 offset:64
	ds_read_b32 v4, v166 offset:128
	ds_read_b32 v5, v166 offset:192
	s_waitcnt lgkmcnt(2)
	v_add_f32_e32 v2, v2, v3
	s_waitcnt lgkmcnt(1)
	v_add_f32_e32 v2, v2, v4
	s_waitcnt lgkmcnt(0)
	v_add_f32_e32 v2, v2, v5
	v_mul_f32_e32 v4, 0x39800000, v2
	v_lshl_add_u64 v[2:3], v[156:157], 2, s[14:15]
	global_store_dword v[2:3], v4, off
	s_branch .LBB1_2
